# v30 + GEMM K-loops: back-to-back s_setprio 0 / s_setprio 1 between the two MFMA blocks of a segment dropped
# baseline (speedup 1.0000x reference)
.LBB0_119:
	ds_read_b128 v[148:151], v153
	ds_read_b128 v[156:159], v153 offset:1024
	ds_read_b128 v[160:163], v153 offset:2048
	ds_read_b128 v[164:167], v153 offset:3072
	ds_read_b128 v[168:171], v154
	ds_read_b128 v[172:175], v154 offset:1024
	ds_read_b128 v[176:179], v154 offset:2048
	ds_read_b128 v[180:183], v154 offset:3072
	s_add_u32 s24, s22, 0xfff80080
	s_addc_u32 s25, s23, -1
	s_cmp_eq_u32 s79, 28
	s_cselect_b32 s27, s15, s25
	s_cselect_b32 s26, s75, s24
	s_cselect_b32 s25, s13, s78
	s_cselect_b32 s24, s76, s77
	s_add_i32 m0, s21, 0xc000
	ds_read_b128 v[184:187], v155
	ds_read_b128 v[188:191], v155 offset:1024
	ds_read_b128 v[192:195], v155 offset:2048
	ds_read_b128 v[196:199], v155 offset:3072
	ds_read_b128 v[200:203], v155 offset:4096
	ds_read_b128 v[204:207], v155 offset:5120
	ds_read_b128 v[208:211], v155 offset:6144
	ds_read_b128 v[212:215], v155 offset:7168
	global_load_lds_dwordx4 v140, s[22:23]
	s_add_i32 m0, s21, 0xe000
	s_nop 0
	global_load_lds_dwordx4 v142, s[22:23]
	s_waitcnt vmcnt(8)
	s_waitcnt lgkmcnt(0)
	s_barrier
	s_setprio 1
	s_waitcnt lgkmcnt(0)
	v_mfma_f32_16x16x32_bf16 v[126:129], v[148:151], v[184:187], v[126:129]
	v_mfma_f32_16x16x32_bf16 v[122:125], v[160:163], v[184:187], v[122:125]
	v_mfma_f32_16x16x32_bf16 v[118:121], v[148:151], v[192:195], v[118:121]
	v_mfma_f32_16x16x32_bf16 v[110:113], v[160:163], v[192:195], v[110:113]
	v_mfma_f32_16x16x32_bf16 v[102:105], v[148:151], v[200:203], v[102:105]
	v_mfma_f32_16x16x32_bf16 v[94:97], v[160:163], v[200:203], v[94:97]
	v_mfma_f32_16x16x32_bf16 v[86:89], v[148:151], v[208:211], v[86:89]
	v_mfma_f32_16x16x32_bf16 v[78:81], v[160:163], v[208:211], v[78:81]
	v_mfma_f32_16x16x32_bf16 v[126:129], v[156:159], v[188:191], v[126:129]
	v_mfma_f32_16x16x32_bf16 v[122:125], v[164:167], v[188:191], v[122:125]
	v_mfma_f32_16x16x32_bf16 v[118:121], v[156:159], v[196:199], v[118:121]
	v_mfma_f32_16x16x32_bf16 v[110:113], v[164:167], v[196:199], v[110:113]
	v_mfma_f32_16x16x32_bf16 v[102:105], v[156:159], v[204:207], v[102:105]
	v_mfma_f32_16x16x32_bf16 v[94:97], v[164:167], v[204:207], v[94:97]
	v_mfma_f32_16x16x32_bf16 v[86:89], v[156:159], v[212:215], v[86:89]
	v_mfma_f32_16x16x32_bf16 v[78:81], v[164:167], v[212:215], v[78:81]
	v_mfma_f32_16x16x32_bf16 v[114:117], v[168:171], v[184:187], v[114:117]
	v_mfma_f32_16x16x32_bf16 v[106:109], v[176:179], v[184:187], v[106:109]
	v_mfma_f32_16x16x32_bf16 v[98:101], v[168:171], v[192:195], v[98:101]
	v_mfma_f32_16x16x32_bf16 v[90:93], v[176:179], v[192:195], v[90:93]
	v_mfma_f32_16x16x32_bf16 v[82:85], v[168:171], v[200:203], v[82:85]
	v_mfma_f32_16x16x32_bf16 v[74:77], v[176:179], v[200:203], v[74:77]
	v_mfma_f32_16x16x32_bf16 v[70:73], v[168:171], v[208:211], v[70:73]
	v_mfma_f32_16x16x32_bf16 v[66:69], v[176:179], v[208:211], v[66:69]
	v_mfma_f32_16x16x32_bf16 v[114:117], v[172:175], v[188:191], v[114:117]
	v_mfma_f32_16x16x32_bf16 v[106:109], v[180:183], v[188:191], v[106:109]
	v_mfma_f32_16x16x32_bf16 v[98:101], v[172:175], v[196:199], v[98:101]
	v_mfma_f32_16x16x32_bf16 v[90:93], v[180:183], v[196:199], v[90:93]
	v_mfma_f32_16x16x32_bf16 v[82:85], v[172:175], v[204:207], v[82:85]
	v_mfma_f32_16x16x32_bf16 v[74:77], v[180:183], v[204:207], v[74:77]
	v_mfma_f32_16x16x32_bf16 v[70:73], v[172:175], v[212:215], v[70:73]
	v_mfma_f32_16x16x32_bf16 v[66:69], v[180:183], v[212:215], v[66:69]
	s_setprio 0
	s_barrier
	s_add_i32 s80, s71, s33
	v_lshl_add_u64 v[216:217], s[24:25], 0, v[136:137]
	s_mov_b32 m0, s80
	ds_read_b128 v[184:187], v155 offset:16384
	ds_read_b128 v[188:191], v155 offset:17408
	ds_read_b128 v[192:195], v155 offset:18432
	ds_read_b128 v[196:199], v155 offset:19456
	ds_read_b128 v[200:203], v155 offset:20480
	ds_read_b128 v[204:207], v155 offset:21504
	ds_read_b128 v[208:211], v155 offset:22528
	ds_read_b128 v[212:215], v155 offset:23552
	global_load_lds_dwordx4 v136, s[24:25]
	s_add_i32 m0, s80, 0x2000
	s_add_u32 s80, s24, 0x80000
	v_lshl_add_u64 v[218:219], s[24:25], 0, v[132:133]
	s_addc_u32 s81, s25, 0
	s_add_i32 s82, s72, s33
	global_load_lds_dwordx4 v132, s[24:25]
	s_mov_b32 m0, s82
	v_lshl_add_u64 v[222:223], s[26:27], 0, v[134:135]
	global_load_lds_dwordx4 v136, s[80:81]
	s_add_i32 m0, s82, 0x2000
	s_nop 0
	global_load_lds_dwordx4 v132, s[80:81]
	v_lshl_add_u64 v[220:221], s[26:27], 0, v[138:139]
	s_mov_b32 m0, s21
	s_nop 0
	global_load_lds_dwordx4 v138, s[26:27]
	s_mov_b32 m0, s36
	s_nop 0
	global_load_lds_dwordx4 v134, s[26:27]
	s_waitcnt vmcnt(8)
	s_waitcnt lgkmcnt(0)
	s_barrier
	s_setprio 1
	s_waitcnt lgkmcnt(0)
	v_mfma_f32_16x16x32_bf16 v[62:65], v[148:151], v[184:187], v[62:65]
	v_mfma_f32_16x16x32_bf16 v[58:61], v[160:163], v[184:187], v[58:61]
	v_mfma_f32_16x16x32_bf16 v[54:57], v[148:151], v[192:195], v[54:57]
	v_mfma_f32_16x16x32_bf16 v[46:49], v[160:163], v[192:195], v[46:49]
	v_mfma_f32_16x16x32_bf16 v[38:41], v[148:151], v[200:203], v[38:41]
	v_mfma_f32_16x16x32_bf16 v[30:33], v[160:163], v[200:203], v[30:33]
	v_mfma_f32_16x16x32_bf16 v[22:25], v[148:151], v[208:211], v[22:25]
	v_mfma_f32_16x16x32_bf16 v[14:17], v[160:163], v[208:211], v[14:17]
	v_mfma_f32_16x16x32_bf16 v[62:65], v[156:159], v[188:191], v[62:65]
	v_mfma_f32_16x16x32_bf16 v[58:61], v[164:167], v[188:191], v[58:61]
	v_mfma_f32_16x16x32_bf16 v[54:57], v[156:159], v[196:199], v[54:57]
	v_mfma_f32_16x16x32_bf16 v[46:49], v[164:167], v[196:199], v[46:49]
	v_mfma_f32_16x16x32_bf16 v[38:41], v[156:159], v[204:207], v[38:41]
	v_mfma_f32_16x16x32_bf16 v[30:33], v[164:167], v[204:207], v[30:33]
	v_mfma_f32_16x16x32_bf16 v[22:25], v[156:159], v[212:215], v[22:25]
	v_mfma_f32_16x16x32_bf16 v[14:17], v[164:167], v[212:215], v[14:17]
	v_mfma_f32_16x16x32_bf16 v[50:53], v[168:171], v[184:187], v[50:53]
	v_mfma_f32_16x16x32_bf16 v[42:45], v[176:179], v[184:187], v[42:45]
	v_mfma_f32_16x16x32_bf16 v[34:37], v[168:171], v[192:195], v[34:37]
	v_mfma_f32_16x16x32_bf16 v[26:29], v[176:179], v[192:195], v[26:29]
	v_mfma_f32_16x16x32_bf16 v[18:21], v[168:171], v[200:203], v[18:21]
	v_mfma_f32_16x16x32_bf16 v[10:13], v[176:179], v[200:203], v[10:13]
	v_mfma_f32_16x16x32_bf16 v[6:9], v[168:171], v[208:211], v[6:9]
	v_mfma_f32_16x16x32_bf16 v[2:5], v[176:179], v[208:211], v[2:5]
	v_mfma_f32_16x16x32_bf16 v[50:53], v[172:175], v[188:191], v[50:53]
	v_mfma_f32_16x16x32_bf16 v[42:45], v[180:183], v[188:191], v[42:45]
	v_mfma_f32_16x16x32_bf16 v[34:37], v[172:175], v[196:199], v[34:37]
	v_mfma_f32_16x16x32_bf16 v[26:29], v[180:183], v[196:199], v[26:29]
	v_mfma_f32_16x16x32_bf16 v[18:21], v[172:175], v[204:207], v[18:21]
	v_mfma_f32_16x16x32_bf16 v[10:13], v[180:183], v[204:207], v[10:13]
	v_mfma_f32_16x16x32_bf16 v[6:9], v[172:175], v[212:215], v[6:9]
	v_mfma_f32_16x16x32_bf16 v[2:5], v[180:183], v[212:215], v[2:5]
	s_setprio 0
	s_barrier
	s_add_i32 s80, 0, 0x18000
	s_add_i32 s81, 0, 0x1c000
	v_add_u32_e32 v164, s80, v131
	v_add_u32_e32 v180, s81, v131
	ds_read_b128 v[148:151], v164
	ds_read_b128 v[156:159], v164 offset:1024
	ds_read_b128 v[160:163], v164 offset:2048
	ds_read_b128 v[164:167], v164 offset:3072
	ds_read_b128 v[168:171], v180
	ds_read_b128 v[172:175], v180 offset:1024
	ds_read_b128 v[176:179], v180 offset:2048
	ds_read_b128 v[180:183], v180 offset:3072
	s_add_u32 s26, s26, 0x80000
	s_addc_u32 s27, s27, 0
	s_mov_b32 m0, s37
	ds_read_b128 v[184:187], v155 offset:32768
	ds_read_b128 v[188:191], v155 offset:33792
	ds_read_b128 v[192:195], v155 offset:34816
	ds_read_b128 v[196:199], v155 offset:35840
	ds_read_b128 v[200:203], v155 offset:36864
	ds_read_b128 v[204:207], v155 offset:37888
	ds_read_b128 v[208:211], v155 offset:38912
	ds_read_b128 v[212:215], v155 offset:39936
	global_load_lds_dwordx4 v138, s[26:27]
	s_mov_b32 m0, s42
	s_nop 0
	global_load_lds_dwordx4 v134, s[26:27]
	s_waitcnt vmcnt(8)
	s_waitcnt lgkmcnt(0)
	s_barrier
	s_setprio 1
	s_waitcnt lgkmcnt(0)
	v_mfma_f32_16x16x32_bf16 v[126:129], v[148:151], v[184:187], v[126:129]
	v_mfma_f32_16x16x32_bf16 v[122:125], v[160:163], v[184:187], v[122:125]
	v_mfma_f32_16x16x32_bf16 v[118:121], v[148:151], v[192:195], v[118:121]
	v_mfma_f32_16x16x32_bf16 v[110:113], v[160:163], v[192:195], v[110:113]
	v_mfma_f32_16x16x32_bf16 v[102:105], v[148:151], v[200:203], v[102:105]
	v_mfma_f32_16x16x32_bf16 v[94:97], v[160:163], v[200:203], v[94:97]
	v_mfma_f32_16x16x32_bf16 v[86:89], v[148:151], v[208:211], v[86:89]
	v_mfma_f32_16x16x32_bf16 v[78:81], v[160:163], v[208:211], v[78:81]
	v_mfma_f32_16x16x32_bf16 v[126:129], v[156:159], v[188:191], v[126:129]
	v_mfma_f32_16x16x32_bf16 v[122:125], v[164:167], v[188:191], v[122:125]
	v_mfma_f32_16x16x32_bf16 v[118:121], v[156:159], v[196:199], v[118:121]
	v_mfma_f32_16x16x32_bf16 v[110:113], v[164:167], v[196:199], v[110:113]
	v_mfma_f32_16x16x32_bf16 v[102:105], v[156:159], v[204:207], v[102:105]
	v_mfma_f32_16x16x32_bf16 v[94:97], v[164:167], v[204:207], v[94:97]
	v_mfma_f32_16x16x32_bf16 v[86:89], v[156:159], v[212:215], v[86:89]
	v_mfma_f32_16x16x32_bf16 v[78:81], v[164:167], v[212:215], v[78:81]
	v_mfma_f32_16x16x32_bf16 v[114:117], v[168:171], v[184:187], v[114:117]
	v_mfma_f32_16x16x32_bf16 v[106:109], v[176:179], v[184:187], v[106:109]
	v_mfma_f32_16x16x32_bf16 v[98:101], v[168:171], v[192:195], v[98:101]
	v_mfma_f32_16x16x32_bf16 v[90:93], v[176:179], v[192:195], v[90:93]
	v_mfma_f32_16x16x32_bf16 v[82:85], v[168:171], v[200:203], v[82:85]
	v_mfma_f32_16x16x32_bf16 v[74:77], v[176:179], v[200:203], v[74:77]
	v_mfma_f32_16x16x32_bf16 v[70:73], v[168:171], v[208:211], v[70:73]
	v_mfma_f32_16x16x32_bf16 v[66:69], v[176:179], v[208:211], v[66:69]
	v_mfma_f32_16x16x32_bf16 v[114:117], v[172:175], v[188:191], v[114:117]
	v_mfma_f32_16x16x32_bf16 v[106:109], v[180:183], v[188:191], v[106:109]
	v_mfma_f32_16x16x32_bf16 v[98:101], v[172:175], v[196:199], v[98:101]
	v_mfma_f32_16x16x32_bf16 v[90:93], v[180:183], v[196:199], v[90:93]
	v_mfma_f32_16x16x32_bf16 v[82:85], v[172:175], v[204:207], v[82:85]
	v_mfma_f32_16x16x32_bf16 v[74:77], v[180:183], v[204:207], v[74:77]
	v_mfma_f32_16x16x32_bf16 v[70:73], v[172:175], v[212:215], v[70:73]
	v_mfma_f32_16x16x32_bf16 v[66:69], v[180:183], v[212:215], v[66:69]
	s_setprio 0
	s_barrier
	s_add_i32 s26, s80, s33
	v_lshl_add_u64 v[216:217], v[216:217], 0, s[8:9]
	s_mov_b32 m0, s26
	ds_read_b128 v[184:187], v155 offset:49152
	ds_read_b128 v[188:191], v155 offset:50176
	ds_read_b128 v[192:195], v155 offset:51200
	ds_read_b128 v[196:199], v155 offset:52224
	ds_read_b128 v[200:203], v155 offset:53248
	ds_read_b128 v[204:207], v155 offset:54272
	ds_read_b128 v[208:211], v155 offset:55296
	ds_read_b128 v[212:215], v155 offset:56320
	global_load_lds_dwordx4 v[216:217], off
	s_add_i32 m0, s26, 0x2000
	s_add_u32 s24, s24, 0x80080
	v_lshl_add_u64 v[216:217], v[218:219], 0, s[8:9]
	s_addc_u32 s25, s25, 0
	s_add_i32 s26, s81, s33
	global_load_lds_dwordx4 v[216:217], off
	s_mov_b32 m0, s26
	s_nop 0
	global_load_lds_dwordx4 v136, s[24:25]
	s_add_i32 m0, s26, 0x2000
	s_nop 0
	global_load_lds_dwordx4 v132, s[24:25]
	v_lshl_add_u64 v[216:217], v[220:221], 0, s[8:9]
	s_mov_b32 m0, s44
	s_nop 0
	global_load_lds_dwordx4 v[216:217], off
	v_lshl_add_u64 v[216:217], v[222:223], 0, s[8:9]
	s_mov_b32 m0, s45
	s_nop 0
	global_load_lds_dwordx4 v[216:217], off
	s_waitcnt vmcnt(8)
	s_waitcnt lgkmcnt(0)
	s_barrier
	s_setprio 1
	s_waitcnt lgkmcnt(0)
	v_mfma_f32_16x16x32_bf16 v[62:65], v[148:151], v[184:187], v[62:65]
	v_mfma_f32_16x16x32_bf16 v[58:61], v[160:163], v[184:187], v[58:61]
	v_mfma_f32_16x16x32_bf16 v[54:57], v[148:151], v[192:195], v[54:57]
	v_mfma_f32_16x16x32_bf16 v[46:49], v[160:163], v[192:195], v[46:49]
	v_mfma_f32_16x16x32_bf16 v[38:41], v[148:151], v[200:203], v[38:41]
	v_mfma_f32_16x16x32_bf16 v[30:33], v[160:163], v[200:203], v[30:33]
	v_mfma_f32_16x16x32_bf16 v[22:25], v[148:151], v[208:211], v[22:25]
	v_mfma_f32_16x16x32_bf16 v[14:17], v[160:163], v[208:211], v[14:17]
	v_mfma_f32_16x16x32_bf16 v[62:65], v[156:159], v[188:191], v[62:65]
	v_mfma_f32_16x16x32_bf16 v[58:61], v[164:167], v[188:191], v[58:61]
	v_mfma_f32_16x16x32_bf16 v[54:57], v[156:159], v[196:199], v[54:57]
	v_mfma_f32_16x16x32_bf16 v[46:49], v[164:167], v[196:199], v[46:49]
	v_mfma_f32_16x16x32_bf16 v[38:41], v[156:159], v[204:207], v[38:41]
	v_mfma_f32_16x16x32_bf16 v[30:33], v[164:167], v[204:207], v[30:33]
	v_mfma_f32_16x16x32_bf16 v[22:25], v[156:159], v[212:215], v[22:25]
	v_mfma_f32_16x16x32_bf16 v[14:17], v[164:167], v[212:215], v[14:17]
	v_mfma_f32_16x16x32_bf16 v[50:53], v[168:171], v[184:187], v[50:53]
	v_mfma_f32_16x16x32_bf16 v[42:45], v[176:179], v[184:187], v[42:45]
	v_mfma_f32_16x16x32_bf16 v[34:37], v[168:171], v[192:195], v[34:37]
	v_mfma_f32_16x16x32_bf16 v[26:29], v[176:179], v[192:195], v[26:29]
	v_mfma_f32_16x16x32_bf16 v[18:21], v[168:171], v[200:203], v[18:21]
	v_mfma_f32_16x16x32_bf16 v[10:13], v[176:179], v[200:203], v[10:13]
	v_mfma_f32_16x16x32_bf16 v[6:9], v[168:171], v[208:211], v[6:9]
	v_mfma_f32_16x16x32_bf16 v[2:5], v[176:179], v[208:211], v[2:5]
	v_mfma_f32_16x16x32_bf16 v[50:53], v[172:175], v[188:191], v[50:53]
	v_mfma_f32_16x16x32_bf16 v[42:45], v[180:183], v[188:191], v[42:45]
	v_mfma_f32_16x16x32_bf16 v[34:37], v[172:175], v[196:199], v[34:37]
	v_mfma_f32_16x16x32_bf16 v[26:29], v[180:183], v[196:199], v[26:29]
	v_mfma_f32_16x16x32_bf16 v[18:21], v[172:175], v[204:207], v[18:21]
	v_mfma_f32_16x16x32_bf16 v[10:13], v[180:183], v[204:207], v[10:13]
	v_mfma_f32_16x16x32_bf16 v[6:9], v[172:175], v[212:215], v[6:9]
	v_mfma_f32_16x16x32_bf16 v[2:5], v[180:183], v[212:215], v[2:5]
	s_setprio 0
	s_barrier
	s_add_i32 s79, s79, 2
	s_add_u32 s22, s22, 0x100
	s_addc_u32 s23, s23, 0
	s_add_u32 s77, s77, 0x100
	s_addc_u32 s78, s78, 0
	s_cmp_gt_u32 s79, 29
	s_cbranch_scc0 .LBB0_119
	s_and_b64 vcc, exec, s[10:11]
	s_cbranch_vccz .LBB0_122
	s_barrier

.LBB0_466:
	ds_read_b128 v[150:153], v211
	ds_read_b128 v[154:157], v211 offset:1024
	ds_read_b128 v[158:161], v211 offset:2048
	ds_read_b128 v[162:165], v211 offset:3072
	ds_read_b128 v[166:169], v212
	ds_read_b128 v[170:173], v212 offset:1024
	ds_read_b128 v[174:177], v212 offset:2048
	ds_read_b128 v[178:181], v212 offset:3072
	s_add_u32 s42, s36, 0xfff80080
	s_addc_u32 s43, s37, -1
	s_cmp_eq_u32 s83, 28
	s_cselect_b32 s45, s1, s43
	s_cselect_b32 s44, s27, s42
	s_cselect_b32 s43, s25, s63
	s_cselect_b32 s42, s35, s62
	s_add_i32 m0, s67, 0xc000
	ds_read_b128 v[182:185], v213
	ds_read_b128 v[186:189], v213 offset:1024
	ds_read_b128 v[190:193], v213 offset:2048
	ds_read_b128 v[194:197], v213 offset:3072
	ds_read_b128 v[198:201], v213 offset:4096
	ds_read_b128 v[202:205], v213 offset:5120
	ds_read_b128 v[218:221], v213 offset:6144
	ds_read_b128 v[222:225], v213 offset:7168
	global_load_lds_dwordx4 v142, s[36:37]
	s_add_i32 m0, s67, 0xe000
	s_nop 0
	global_load_lds_dwordx4 v144, s[36:37]
	s_waitcnt vmcnt(8)
	s_waitcnt lgkmcnt(0)
	s_barrier
	s_setprio 1
	s_waitcnt lgkmcnt(0)
	v_mfma_f32_16x16x32_bf16 v[126:129], v[150:153], v[182:185], v[126:129]
	v_mfma_f32_16x16x32_bf16 v[122:125], v[158:161], v[182:185], v[122:125]
	v_mfma_f32_16x16x32_bf16 v[110:113], v[150:153], v[190:193], v[110:113]
	v_mfma_f32_16x16x32_bf16 v[106:109], v[158:161], v[190:193], v[106:109]
	v_mfma_f32_16x16x32_bf16 v[94:97], v[150:153], v[198:201], v[94:97]
	v_mfma_f32_16x16x32_bf16 v[90:93], v[158:161], v[198:201], v[90:93]
	v_mfma_f32_16x16x32_bf16 v[78:81], v[150:153], v[218:221], v[78:81]
	v_mfma_f32_16x16x32_bf16 v[74:77], v[158:161], v[218:221], v[74:77]
	v_mfma_f32_16x16x32_bf16 v[126:129], v[154:157], v[186:189], v[126:129]
	v_mfma_f32_16x16x32_bf16 v[122:125], v[162:165], v[186:189], v[122:125]
	v_mfma_f32_16x16x32_bf16 v[110:113], v[154:157], v[194:197], v[110:113]
	v_mfma_f32_16x16x32_bf16 v[106:109], v[162:165], v[194:197], v[106:109]
	v_mfma_f32_16x16x32_bf16 v[94:97], v[154:157], v[202:205], v[94:97]
	v_mfma_f32_16x16x32_bf16 v[90:93], v[162:165], v[202:205], v[90:93]
	v_mfma_f32_16x16x32_bf16 v[78:81], v[154:157], v[222:225], v[78:81]
	v_mfma_f32_16x16x32_bf16 v[74:77], v[162:165], v[222:225], v[74:77]
	v_mfma_f32_16x16x32_bf16 v[118:121], v[166:169], v[182:185], v[118:121]
	v_mfma_f32_16x16x32_bf16 v[114:117], v[174:177], v[182:185], v[114:117]
	v_mfma_f32_16x16x32_bf16 v[102:105], v[166:169], v[190:193], v[102:105]
	v_mfma_f32_16x16x32_bf16 v[98:101], v[174:177], v[190:193], v[98:101]
	v_mfma_f32_16x16x32_bf16 v[86:89], v[166:169], v[198:201], v[86:89]
	v_mfma_f32_16x16x32_bf16 v[82:85], v[174:177], v[198:201], v[82:85]
	v_mfma_f32_16x16x32_bf16 v[70:73], v[166:169], v[218:221], v[70:73]
	v_mfma_f32_16x16x32_bf16 v[66:69], v[174:177], v[218:221], v[66:69]
	v_mfma_f32_16x16x32_bf16 v[118:121], v[170:173], v[186:189], v[118:121]
	v_mfma_f32_16x16x32_bf16 v[114:117], v[178:181], v[186:189], v[114:117]
	v_mfma_f32_16x16x32_bf16 v[102:105], v[170:173], v[194:197], v[102:105]
	v_mfma_f32_16x16x32_bf16 v[98:101], v[178:181], v[194:197], v[98:101]
	v_mfma_f32_16x16x32_bf16 v[86:89], v[170:173], v[202:205], v[86:89]
	v_mfma_f32_16x16x32_bf16 v[82:85], v[178:181], v[202:205], v[82:85]
	v_mfma_f32_16x16x32_bf16 v[70:73], v[170:173], v[222:225], v[70:73]
	v_mfma_f32_16x16x32_bf16 v[66:69], v[178:181], v[222:225], v[66:69]
	s_setprio 0
	s_barrier
	s_add_i32 s84, s79, s66
	v_lshl_add_u64 v[226:227], s[42:43], 0, v[132:133]
	s_mov_b32 m0, s84
	ds_read_b128 v[182:185], v213 offset:16384
	ds_read_b128 v[186:189], v213 offset:17408
	ds_read_b128 v[190:193], v213 offset:18432
	ds_read_b128 v[194:197], v213 offset:19456
	ds_read_b128 v[198:201], v213 offset:20480
	ds_read_b128 v[202:205], v213 offset:21504
	ds_read_b128 v[218:221], v213 offset:22528
	ds_read_b128 v[222:225], v213 offset:23552
	global_load_lds_dwordx4 v132, s[42:43]
	s_add_i32 m0, s84, 0x2000
	s_add_u32 s84, s42, 0x80000
	v_lshl_add_u64 v[228:229], s[42:43], 0, v[136:137]
	s_addc_u32 s85, s43, 0
	s_add_i32 s86, s80, s66
	global_load_lds_dwordx4 v136, s[42:43]
	s_mov_b32 m0, s86
	v_lshl_add_u64 v[232:233], s[44:45], 0, v[134:135]
	global_load_lds_dwordx4 v132, s[84:85]
	s_add_i32 m0, s86, 0x2000
	s_nop 0
	global_load_lds_dwordx4 v136, s[84:85]
	v_lshl_add_u64 v[230:231], s[44:45], 0, v[130:131]
	s_mov_b32 m0, s67
	s_nop 0
	global_load_lds_dwordx4 v130, s[44:45]
	s_mov_b32 m0, s68
	s_nop 0
	global_load_lds_dwordx4 v134, s[44:45]
	s_waitcnt vmcnt(8)
	s_waitcnt lgkmcnt(0)
	s_barrier
	s_setprio 1
	s_waitcnt lgkmcnt(0)
	v_mfma_f32_16x16x32_bf16 v[62:65], v[150:153], v[182:185], v[62:65]
	v_mfma_f32_16x16x32_bf16 v[58:61], v[158:161], v[182:185], v[58:61]
	v_mfma_f32_16x16x32_bf16 v[46:49], v[150:153], v[190:193], v[46:49]
	v_mfma_f32_16x16x32_bf16 v[42:45], v[158:161], v[190:193], v[42:45]
	v_mfma_f32_16x16x32_bf16 v[30:33], v[150:153], v[198:201], v[30:33]
	v_mfma_f32_16x16x32_bf16 v[26:29], v[158:161], v[198:201], v[26:29]
	v_mfma_f32_16x16x32_bf16 v[14:17], v[150:153], v[218:221], v[14:17]
	v_mfma_f32_16x16x32_bf16 v[10:13], v[158:161], v[218:221], v[10:13]
	v_mfma_f32_16x16x32_bf16 v[62:65], v[154:157], v[186:189], v[62:65]
	v_mfma_f32_16x16x32_bf16 v[58:61], v[162:165], v[186:189], v[58:61]
	v_mfma_f32_16x16x32_bf16 v[46:49], v[154:157], v[194:197], v[46:49]
	v_mfma_f32_16x16x32_bf16 v[42:45], v[162:165], v[194:197], v[42:45]
	v_mfma_f32_16x16x32_bf16 v[30:33], v[154:157], v[202:205], v[30:33]
	v_mfma_f32_16x16x32_bf16 v[26:29], v[162:165], v[202:205], v[26:29]
	v_mfma_f32_16x16x32_bf16 v[14:17], v[154:157], v[222:225], v[14:17]
	v_mfma_f32_16x16x32_bf16 v[10:13], v[162:165], v[222:225], v[10:13]
	v_mfma_f32_16x16x32_bf16 v[54:57], v[166:169], v[182:185], v[54:57]
	v_mfma_f32_16x16x32_bf16 v[50:53], v[174:177], v[182:185], v[50:53]
	v_mfma_f32_16x16x32_bf16 v[38:41], v[166:169], v[190:193], v[38:41]
	v_mfma_f32_16x16x32_bf16 v[34:37], v[174:177], v[190:193], v[34:37]
	v_mfma_f32_16x16x32_bf16 v[22:25], v[166:169], v[198:201], v[22:25]
	v_mfma_f32_16x16x32_bf16 v[18:21], v[174:177], v[198:201], v[18:21]
	v_mfma_f32_16x16x32_bf16 v[6:9], v[166:169], v[218:221], v[6:9]
	v_mfma_f32_16x16x32_bf16 v[2:5], v[174:177], v[218:221], v[2:5]
	v_mfma_f32_16x16x32_bf16 v[54:57], v[170:173], v[186:189], v[54:57]
	v_mfma_f32_16x16x32_bf16 v[50:53], v[178:181], v[186:189], v[50:53]
	v_mfma_f32_16x16x32_bf16 v[38:41], v[170:173], v[194:197], v[38:41]
	v_mfma_f32_16x16x32_bf16 v[34:37], v[178:181], v[194:197], v[34:37]
	v_mfma_f32_16x16x32_bf16 v[22:25], v[170:173], v[202:205], v[22:25]
	v_mfma_f32_16x16x32_bf16 v[18:21], v[178:181], v[202:205], v[18:21]
	v_mfma_f32_16x16x32_bf16 v[6:9], v[170:173], v[222:225], v[6:9]
	v_mfma_f32_16x16x32_bf16 v[2:5], v[178:181], v[222:225], v[2:5]
	s_setprio 0
	s_barrier
	s_add_i32 s84, 0, 0x18000
	v_add_u32_e32 v139, s84, v206
	s_add_i32 s85, 0, 0x1c000
	ds_read_b128 v[150:153], v139
	ds_read_b128 v[154:157], v139 offset:1024
	ds_read_b128 v[158:161], v139 offset:2048
	ds_read_b128 v[162:165], v139 offset:3072
	v_add_u32_e32 v139, s85, v206
	ds_read_b128 v[166:169], v139
	ds_read_b128 v[170:173], v139 offset:1024
	ds_read_b128 v[174:177], v139 offset:2048
	ds_read_b128 v[178:181], v139 offset:3072
	s_add_u32 s44, s44, 0x80000
	s_addc_u32 s45, s45, 0
	s_mov_b32 m0, s69
	ds_read_b128 v[182:185], v213 offset:32768
	ds_read_b128 v[186:189], v213 offset:33792
	ds_read_b128 v[190:193], v213 offset:34816
	ds_read_b128 v[194:197], v213 offset:35840
	ds_read_b128 v[198:201], v213 offset:36864
	ds_read_b128 v[202:205], v213 offset:37888
	ds_read_b128 v[218:221], v213 offset:38912
	ds_read_b128 v[222:225], v213 offset:39936
	global_load_lds_dwordx4 v130, s[44:45]
	s_mov_b32 m0, s70
	s_nop 0
	global_load_lds_dwordx4 v134, s[44:45]
	s_waitcnt vmcnt(8)
	s_waitcnt lgkmcnt(0)
	s_barrier
	s_setprio 1
	s_waitcnt lgkmcnt(0)
	v_mfma_f32_16x16x32_bf16 v[126:129], v[150:153], v[182:185], v[126:129]
	v_mfma_f32_16x16x32_bf16 v[122:125], v[158:161], v[182:185], v[122:125]
	v_mfma_f32_16x16x32_bf16 v[110:113], v[150:153], v[190:193], v[110:113]
	v_mfma_f32_16x16x32_bf16 v[106:109], v[158:161], v[190:193], v[106:109]
	v_mfma_f32_16x16x32_bf16 v[94:97], v[150:153], v[198:201], v[94:97]
	v_mfma_f32_16x16x32_bf16 v[90:93], v[158:161], v[198:201], v[90:93]
	v_mfma_f32_16x16x32_bf16 v[78:81], v[150:153], v[218:221], v[78:81]
	v_mfma_f32_16x16x32_bf16 v[74:77], v[158:161], v[218:221], v[74:77]
	v_mfma_f32_16x16x32_bf16 v[126:129], v[154:157], v[186:189], v[126:129]
	v_mfma_f32_16x16x32_bf16 v[122:125], v[162:165], v[186:189], v[122:125]
	v_mfma_f32_16x16x32_bf16 v[110:113], v[154:157], v[194:197], v[110:113]
	v_mfma_f32_16x16x32_bf16 v[106:109], v[162:165], v[194:197], v[106:109]
	v_mfma_f32_16x16x32_bf16 v[94:97], v[154:157], v[202:205], v[94:97]
	v_mfma_f32_16x16x32_bf16 v[90:93], v[162:165], v[202:205], v[90:93]
	v_mfma_f32_16x16x32_bf16 v[78:81], v[154:157], v[222:225], v[78:81]
	v_mfma_f32_16x16x32_bf16 v[74:77], v[162:165], v[222:225], v[74:77]
	v_mfma_f32_16x16x32_bf16 v[118:121], v[166:169], v[182:185], v[118:121]
	v_mfma_f32_16x16x32_bf16 v[114:117], v[174:177], v[182:185], v[114:117]
	v_mfma_f32_16x16x32_bf16 v[102:105], v[166:169], v[190:193], v[102:105]
	v_mfma_f32_16x16x32_bf16 v[98:101], v[174:177], v[190:193], v[98:101]
	v_mfma_f32_16x16x32_bf16 v[86:89], v[166:169], v[198:201], v[86:89]
	v_mfma_f32_16x16x32_bf16 v[82:85], v[174:177], v[198:201], v[82:85]
	v_mfma_f32_16x16x32_bf16 v[70:73], v[166:169], v[218:221], v[70:73]
	v_mfma_f32_16x16x32_bf16 v[66:69], v[174:177], v[218:221], v[66:69]
	v_mfma_f32_16x16x32_bf16 v[118:121], v[170:173], v[186:189], v[118:121]
	v_mfma_f32_16x16x32_bf16 v[114:117], v[178:181], v[186:189], v[114:117]
	v_mfma_f32_16x16x32_bf16 v[102:105], v[170:173], v[194:197], v[102:105]
	v_mfma_f32_16x16x32_bf16 v[98:101], v[178:181], v[194:197], v[98:101]
	v_mfma_f32_16x16x32_bf16 v[86:89], v[170:173], v[202:205], v[86:89]
	v_mfma_f32_16x16x32_bf16 v[82:85], v[178:181], v[202:205], v[82:85]
	v_mfma_f32_16x16x32_bf16 v[70:73], v[170:173], v[222:225], v[70:73]
	v_mfma_f32_16x16x32_bf16 v[66:69], v[178:181], v[222:225], v[66:69]
	s_setprio 0
	s_barrier
	s_add_i32 s44, s84, s66
	v_lshl_add_u64 v[226:227], v[226:227], 0, s[18:19]
	s_mov_b32 m0, s44
	ds_read_b128 v[182:185], v213 offset:49152
	ds_read_b128 v[186:189], v213 offset:50176
	ds_read_b128 v[190:193], v213 offset:51200
	ds_read_b128 v[194:197], v213 offset:52224
	ds_read_b128 v[198:201], v213 offset:53248
	ds_read_b128 v[202:205], v213 offset:54272
	ds_read_b128 v[218:221], v213 offset:55296
	ds_read_b128 v[222:225], v213 offset:56320
	global_load_lds_dwordx4 v[226:227], off
	s_add_i32 m0, s44, 0x2000
	s_add_u32 s42, s42, 0x80080
	v_lshl_add_u64 v[226:227], v[228:229], 0, s[18:19]
	s_addc_u32 s43, s43, 0
	s_add_i32 s44, s85, s66
	global_load_lds_dwordx4 v[226:227], off
	s_mov_b32 m0, s44
	s_nop 0
	global_load_lds_dwordx4 v132, s[42:43]
	s_add_i32 m0, s44, 0x2000
	s_nop 0
	global_load_lds_dwordx4 v136, s[42:43]
	v_lshl_add_u64 v[226:227], v[230:231], 0, s[18:19]
	s_mov_b32 m0, s74
	s_nop 0
	global_load_lds_dwordx4 v[226:227], off
	v_lshl_add_u64 v[226:227], v[232:233], 0, s[18:19]
	s_mov_b32 m0, s75
	s_nop 0
	global_load_lds_dwordx4 v[226:227], off
	s_waitcnt vmcnt(8)
	s_waitcnt lgkmcnt(0)
	s_barrier
	s_setprio 1
	s_waitcnt lgkmcnt(0)
	v_mfma_f32_16x16x32_bf16 v[62:65], v[150:153], v[182:185], v[62:65]
	v_mfma_f32_16x16x32_bf16 v[58:61], v[158:161], v[182:185], v[58:61]
	v_mfma_f32_16x16x32_bf16 v[46:49], v[150:153], v[190:193], v[46:49]
	v_mfma_f32_16x16x32_bf16 v[42:45], v[158:161], v[190:193], v[42:45]
	v_mfma_f32_16x16x32_bf16 v[30:33], v[150:153], v[198:201], v[30:33]
	v_mfma_f32_16x16x32_bf16 v[26:29], v[158:161], v[198:201], v[26:29]
	v_mfma_f32_16x16x32_bf16 v[14:17], v[150:153], v[218:221], v[14:17]
	v_mfma_f32_16x16x32_bf16 v[10:13], v[158:161], v[218:221], v[10:13]
	v_mfma_f32_16x16x32_bf16 v[62:65], v[154:157], v[186:189], v[62:65]
	v_mfma_f32_16x16x32_bf16 v[58:61], v[162:165], v[186:189], v[58:61]
	v_mfma_f32_16x16x32_bf16 v[46:49], v[154:157], v[194:197], v[46:49]
	v_mfma_f32_16x16x32_bf16 v[42:45], v[162:165], v[194:197], v[42:45]
	v_mfma_f32_16x16x32_bf16 v[30:33], v[154:157], v[202:205], v[30:33]
	v_mfma_f32_16x16x32_bf16 v[26:29], v[162:165], v[202:205], v[26:29]
	v_mfma_f32_16x16x32_bf16 v[14:17], v[154:157], v[222:225], v[14:17]
	v_mfma_f32_16x16x32_bf16 v[10:13], v[162:165], v[222:225], v[10:13]
	v_mfma_f32_16x16x32_bf16 v[54:57], v[166:169], v[182:185], v[54:57]
	v_mfma_f32_16x16x32_bf16 v[50:53], v[174:177], v[182:185], v[50:53]
	v_mfma_f32_16x16x32_bf16 v[38:41], v[166:169], v[190:193], v[38:41]
	v_mfma_f32_16x16x32_bf16 v[34:37], v[174:177], v[190:193], v[34:37]
	v_mfma_f32_16x16x32_bf16 v[22:25], v[166:169], v[198:201], v[22:25]
	v_mfma_f32_16x16x32_bf16 v[18:21], v[174:177], v[198:201], v[18:21]
	v_mfma_f32_16x16x32_bf16 v[6:9], v[166:169], v[218:221], v[6:9]
	v_mfma_f32_16x16x32_bf16 v[2:5], v[174:177], v[218:221], v[2:5]
	v_mfma_f32_16x16x32_bf16 v[54:57], v[170:173], v[186:189], v[54:57]
	v_mfma_f32_16x16x32_bf16 v[50:53], v[178:181], v[186:189], v[50:53]
	v_mfma_f32_16x16x32_bf16 v[38:41], v[170:173], v[194:197], v[38:41]
	v_mfma_f32_16x16x32_bf16 v[34:37], v[178:181], v[194:197], v[34:37]
	v_mfma_f32_16x16x32_bf16 v[22:25], v[170:173], v[202:205], v[22:25]
	v_mfma_f32_16x16x32_bf16 v[18:21], v[178:181], v[202:205], v[18:21]
	v_mfma_f32_16x16x32_bf16 v[6:9], v[170:173], v[222:225], v[6:9]
	v_mfma_f32_16x16x32_bf16 v[2:5], v[178:181], v[222:225], v[2:5]
	s_setprio 0
	s_barrier
	s_add_i32 s83, s83, 2
	s_add_u32 s36, s36, 0x100
	s_addc_u32 s37, s37, 0
	s_add_u32 s62, s62, 0x100
	s_addc_u32 s63, s63, 0
	s_cmp_gt_u32 s83, 29
	s_cbranch_scc0 .LBB0_466
	s_and_b64 vcc, exec, s[20:21]
	s_cbranch_vccz .LBB0_469
	s_barrier

.LBB0_574:
	ds_read_b128 v[146:149], v152
	ds_read_b128 v[156:159], v152 offset:1024
	ds_read_b128 v[160:163], v152 offset:2048
	ds_read_b128 v[164:167], v152 offset:3072
	ds_read_b128 v[168:171], v153
	ds_read_b128 v[172:175], v153 offset:1024
	ds_read_b128 v[176:179], v153 offset:2048
	ds_read_b128 v[180:183], v153 offset:3072
	s_add_u32 s24, s22, 0xfff80080
	s_addc_u32 s25, s23, -1
	s_cmp_eq_u32 s69, 28
	s_cselect_b32 s27, s15, s25
	s_cselect_b32 s26, s65, s24
	s_cselect_b32 s25, s13, s68
	s_cselect_b32 s24, s66, s67
	s_add_i32 m0, s21, 0xc000
	ds_read_b128 v[184:187], v154
	ds_read_b128 v[188:191], v154 offset:1024
	ds_read_b128 v[192:195], v154 offset:2048
	ds_read_b128 v[196:199], v154 offset:3072
	ds_read_b128 v[200:203], v154 offset:4096
	ds_read_b128 v[204:207], v154 offset:5120
	ds_read_b128 v[208:211], v154 offset:6144
	ds_read_b128 v[212:215], v154 offset:7168
	global_load_lds_dwordx4 v138, s[22:23]
	s_add_i32 m0, s21, 0xe000
	s_nop 0
	global_load_lds_dwordx4 v140, s[22:23]
	s_waitcnt vmcnt(8)
	s_waitcnt lgkmcnt(0)
	s_barrier
	s_setprio 1
	s_waitcnt lgkmcnt(0)
	v_mfma_f32_16x16x32_bf16 v[126:129], v[146:149], v[184:187], v[126:129]
	v_mfma_f32_16x16x32_bf16 v[122:125], v[160:163], v[184:187], v[122:125]
	v_mfma_f32_16x16x32_bf16 v[110:113], v[146:149], v[192:195], v[110:113]
	v_mfma_f32_16x16x32_bf16 v[106:109], v[160:163], v[192:195], v[106:109]
	v_mfma_f32_16x16x32_bf16 v[94:97], v[146:149], v[200:203], v[94:97]
	v_mfma_f32_16x16x32_bf16 v[90:93], v[160:163], v[200:203], v[90:93]
	v_mfma_f32_16x16x32_bf16 v[78:81], v[146:149], v[208:211], v[78:81]
	v_mfma_f32_16x16x32_bf16 v[74:77], v[160:163], v[208:211], v[74:77]
	v_mfma_f32_16x16x32_bf16 v[126:129], v[156:159], v[188:191], v[126:129]
	v_mfma_f32_16x16x32_bf16 v[122:125], v[164:167], v[188:191], v[122:125]
	v_mfma_f32_16x16x32_bf16 v[110:113], v[156:159], v[196:199], v[110:113]
	v_mfma_f32_16x16x32_bf16 v[106:109], v[164:167], v[196:199], v[106:109]
	v_mfma_f32_16x16x32_bf16 v[94:97], v[156:159], v[204:207], v[94:97]
	v_mfma_f32_16x16x32_bf16 v[90:93], v[164:167], v[204:207], v[90:93]
	v_mfma_f32_16x16x32_bf16 v[78:81], v[156:159], v[212:215], v[78:81]
	v_mfma_f32_16x16x32_bf16 v[74:77], v[164:167], v[212:215], v[74:77]
	v_mfma_f32_16x16x32_bf16 v[118:121], v[168:171], v[184:187], v[118:121]
	v_mfma_f32_16x16x32_bf16 v[114:117], v[176:179], v[184:187], v[114:117]
	v_mfma_f32_16x16x32_bf16 v[102:105], v[168:171], v[192:195], v[102:105]
	v_mfma_f32_16x16x32_bf16 v[98:101], v[176:179], v[192:195], v[98:101]
	v_mfma_f32_16x16x32_bf16 v[86:89], v[168:171], v[200:203], v[86:89]
	v_mfma_f32_16x16x32_bf16 v[82:85], v[176:179], v[200:203], v[82:85]
	v_mfma_f32_16x16x32_bf16 v[70:73], v[168:171], v[208:211], v[70:73]
	v_mfma_f32_16x16x32_bf16 v[66:69], v[176:179], v[208:211], v[66:69]
	v_mfma_f32_16x16x32_bf16 v[118:121], v[172:175], v[188:191], v[118:121]
	v_mfma_f32_16x16x32_bf16 v[114:117], v[180:183], v[188:191], v[114:117]
	v_mfma_f32_16x16x32_bf16 v[102:105], v[172:175], v[196:199], v[102:105]
	v_mfma_f32_16x16x32_bf16 v[98:101], v[180:183], v[196:199], v[98:101]
	v_mfma_f32_16x16x32_bf16 v[86:89], v[172:175], v[204:207], v[86:89]
	v_mfma_f32_16x16x32_bf16 v[82:85], v[180:183], v[204:207], v[82:85]
	v_mfma_f32_16x16x32_bf16 v[70:73], v[172:175], v[212:215], v[70:73]
	v_mfma_f32_16x16x32_bf16 v[66:69], v[180:183], v[212:215], v[66:69]
	s_setprio 0
	s_barrier
	s_add_i32 s70, s61, s33
	v_lshl_add_u64 v[216:217], s[24:25], 0, v[134:135]
	s_mov_b32 m0, s70
	ds_read_b128 v[184:187], v154 offset:16384
	ds_read_b128 v[188:191], v154 offset:17408
	ds_read_b128 v[192:195], v154 offset:18432
	ds_read_b128 v[196:199], v154 offset:19456
	ds_read_b128 v[200:203], v154 offset:20480
	ds_read_b128 v[204:207], v154 offset:21504
	ds_read_b128 v[208:211], v154 offset:22528
	ds_read_b128 v[212:215], v154 offset:23552
	global_load_lds_dwordx4 v134, s[24:25]
	s_add_i32 m0, s70, 0x2000
	s_add_u32 s70, s24, 0x80000
	v_lshl_add_u64 v[218:219], s[24:25], 0, v[130:131]
	s_addc_u32 s71, s25, 0
	s_add_i32 s72, s62, s33
	global_load_lds_dwordx4 v130, s[24:25]
	s_mov_b32 m0, s72
	v_lshl_add_u64 v[222:223], s[26:27], 0, v[132:133]
	global_load_lds_dwordx4 v134, s[70:71]
	s_add_i32 m0, s72, 0x2000
	s_nop 0
	global_load_lds_dwordx4 v130, s[70:71]
	v_lshl_add_u64 v[220:221], s[26:27], 0, v[136:137]
	s_mov_b32 m0, s21
	s_nop 0
	global_load_lds_dwordx4 v136, s[26:27]
	s_mov_b32 m0, s36
	s_nop 0
	global_load_lds_dwordx4 v132, s[26:27]
	s_waitcnt vmcnt(8)
	s_waitcnt lgkmcnt(0)
	s_barrier
	s_setprio 1
	s_waitcnt lgkmcnt(0)
	v_mfma_f32_16x16x32_bf16 v[62:65], v[146:149], v[184:187], v[62:65]
	v_mfma_f32_16x16x32_bf16 v[58:61], v[160:163], v[184:187], v[58:61]
	v_mfma_f32_16x16x32_bf16 v[46:49], v[146:149], v[192:195], v[46:49]
	v_mfma_f32_16x16x32_bf16 v[42:45], v[160:163], v[192:195], v[42:45]
	v_mfma_f32_16x16x32_bf16 v[30:33], v[146:149], v[200:203], v[30:33]
	v_mfma_f32_16x16x32_bf16 v[26:29], v[160:163], v[200:203], v[26:29]
	v_mfma_f32_16x16x32_bf16 v[14:17], v[146:149], v[208:211], v[14:17]
	v_mfma_f32_16x16x32_bf16 v[10:13], v[160:163], v[208:211], v[10:13]
	v_mfma_f32_16x16x32_bf16 v[62:65], v[156:159], v[188:191], v[62:65]
	v_mfma_f32_16x16x32_bf16 v[58:61], v[164:167], v[188:191], v[58:61]
	v_mfma_f32_16x16x32_bf16 v[46:49], v[156:159], v[196:199], v[46:49]
	v_mfma_f32_16x16x32_bf16 v[42:45], v[164:167], v[196:199], v[42:45]
	v_mfma_f32_16x16x32_bf16 v[30:33], v[156:159], v[204:207], v[30:33]
	v_mfma_f32_16x16x32_bf16 v[26:29], v[164:167], v[204:207], v[26:29]
	v_mfma_f32_16x16x32_bf16 v[14:17], v[156:159], v[212:215], v[14:17]
	v_mfma_f32_16x16x32_bf16 v[10:13], v[164:167], v[212:215], v[10:13]
	v_mfma_f32_16x16x32_bf16 v[54:57], v[168:171], v[184:187], v[54:57]
	v_mfma_f32_16x16x32_bf16 v[50:53], v[176:179], v[184:187], v[50:53]
	v_mfma_f32_16x16x32_bf16 v[38:41], v[168:171], v[192:195], v[38:41]
	v_mfma_f32_16x16x32_bf16 v[34:37], v[176:179], v[192:195], v[34:37]
	v_mfma_f32_16x16x32_bf16 v[22:25], v[168:171], v[200:203], v[22:25]
	v_mfma_f32_16x16x32_bf16 v[18:21], v[176:179], v[200:203], v[18:21]
	v_mfma_f32_16x16x32_bf16 v[6:9], v[168:171], v[208:211], v[6:9]
	v_mfma_f32_16x16x32_bf16 v[2:5], v[176:179], v[208:211], v[2:5]
	v_mfma_f32_16x16x32_bf16 v[54:57], v[172:175], v[188:191], v[54:57]
	v_mfma_f32_16x16x32_bf16 v[50:53], v[180:183], v[188:191], v[50:53]
	v_mfma_f32_16x16x32_bf16 v[38:41], v[172:175], v[196:199], v[38:41]
	v_mfma_f32_16x16x32_bf16 v[34:37], v[180:183], v[196:199], v[34:37]
	v_mfma_f32_16x16x32_bf16 v[22:25], v[172:175], v[204:207], v[22:25]
	v_mfma_f32_16x16x32_bf16 v[18:21], v[180:183], v[204:207], v[18:21]
	v_mfma_f32_16x16x32_bf16 v[6:9], v[172:175], v[212:215], v[6:9]
	v_mfma_f32_16x16x32_bf16 v[2:5], v[180:183], v[212:215], v[2:5]
	s_setprio 0
	s_barrier
	s_add_i32 s70, 0, 0x18000
	v_add_u32_e32 v155, s70, v150
	s_add_i32 s71, 0, 0x1c000
	ds_read_b128 v[146:149], v155
	ds_read_b128 v[156:159], v155 offset:1024
	ds_read_b128 v[160:163], v155 offset:2048
	ds_read_b128 v[164:167], v155 offset:3072
	v_add_u32_e32 v155, s71, v150
	ds_read_b128 v[168:171], v155
	ds_read_b128 v[172:175], v155 offset:1024
	ds_read_b128 v[176:179], v155 offset:2048
	ds_read_b128 v[180:183], v155 offset:3072
	s_add_u32 s26, s26, 0x80000
	s_addc_u32 s27, s27, 0
	s_mov_b32 m0, s37
	ds_read_b128 v[184:187], v154 offset:32768
	ds_read_b128 v[188:191], v154 offset:33792
	ds_read_b128 v[192:195], v154 offset:34816
	ds_read_b128 v[196:199], v154 offset:35840
	ds_read_b128 v[200:203], v154 offset:36864
	ds_read_b128 v[204:207], v154 offset:37888
	ds_read_b128 v[208:211], v154 offset:38912
	ds_read_b128 v[212:215], v154 offset:39936
	global_load_lds_dwordx4 v136, s[26:27]
	s_mov_b32 m0, s42
	s_nop 0
	global_load_lds_dwordx4 v132, s[26:27]
	s_waitcnt vmcnt(8)
	s_waitcnt lgkmcnt(0)
	s_barrier
	s_setprio 1
	s_waitcnt lgkmcnt(0)
	v_mfma_f32_16x16x32_bf16 v[126:129], v[146:149], v[184:187], v[126:129]
	v_mfma_f32_16x16x32_bf16 v[122:125], v[160:163], v[184:187], v[122:125]
	v_mfma_f32_16x16x32_bf16 v[110:113], v[146:149], v[192:195], v[110:113]
	v_mfma_f32_16x16x32_bf16 v[106:109], v[160:163], v[192:195], v[106:109]
	v_mfma_f32_16x16x32_bf16 v[94:97], v[146:149], v[200:203], v[94:97]
	v_mfma_f32_16x16x32_bf16 v[90:93], v[160:163], v[200:203], v[90:93]
	v_mfma_f32_16x16x32_bf16 v[78:81], v[146:149], v[208:211], v[78:81]
	v_mfma_f32_16x16x32_bf16 v[74:77], v[160:163], v[208:211], v[74:77]
	v_mfma_f32_16x16x32_bf16 v[126:129], v[156:159], v[188:191], v[126:129]
	v_mfma_f32_16x16x32_bf16 v[122:125], v[164:167], v[188:191], v[122:125]
	v_mfma_f32_16x16x32_bf16 v[110:113], v[156:159], v[196:199], v[110:113]
	v_mfma_f32_16x16x32_bf16 v[106:109], v[164:167], v[196:199], v[106:109]
	v_mfma_f32_16x16x32_bf16 v[94:97], v[156:159], v[204:207], v[94:97]
	v_mfma_f32_16x16x32_bf16 v[90:93], v[164:167], v[204:207], v[90:93]
	v_mfma_f32_16x16x32_bf16 v[78:81], v[156:159], v[212:215], v[78:81]
	v_mfma_f32_16x16x32_bf16 v[74:77], v[164:167], v[212:215], v[74:77]
	v_mfma_f32_16x16x32_bf16 v[118:121], v[168:171], v[184:187], v[118:121]
	v_mfma_f32_16x16x32_bf16 v[114:117], v[176:179], v[184:187], v[114:117]
	v_mfma_f32_16x16x32_bf16 v[102:105], v[168:171], v[192:195], v[102:105]
	v_mfma_f32_16x16x32_bf16 v[98:101], v[176:179], v[192:195], v[98:101]
	v_mfma_f32_16x16x32_bf16 v[86:89], v[168:171], v[200:203], v[86:89]
	v_mfma_f32_16x16x32_bf16 v[82:85], v[176:179], v[200:203], v[82:85]
	v_mfma_f32_16x16x32_bf16 v[70:73], v[168:171], v[208:211], v[70:73]
	v_mfma_f32_16x16x32_bf16 v[66:69], v[176:179], v[208:211], v[66:69]
	v_mfma_f32_16x16x32_bf16 v[118:121], v[172:175], v[188:191], v[118:121]
	v_mfma_f32_16x16x32_bf16 v[114:117], v[180:183], v[188:191], v[114:117]
	v_mfma_f32_16x16x32_bf16 v[102:105], v[172:175], v[196:199], v[102:105]
	v_mfma_f32_16x16x32_bf16 v[98:101], v[180:183], v[196:199], v[98:101]
	v_mfma_f32_16x16x32_bf16 v[86:89], v[172:175], v[204:207], v[86:89]
	v_mfma_f32_16x16x32_bf16 v[82:85], v[180:183], v[204:207], v[82:85]
	v_mfma_f32_16x16x32_bf16 v[70:73], v[172:175], v[212:215], v[70:73]
	v_mfma_f32_16x16x32_bf16 v[66:69], v[180:183], v[212:215], v[66:69]
	s_setprio 0
	s_barrier
	s_add_i32 s26, s70, s33
	v_lshl_add_u64 v[216:217], v[216:217], 0, s[8:9]
	s_mov_b32 m0, s26
	ds_read_b128 v[184:187], v154 offset:49152
	ds_read_b128 v[188:191], v154 offset:50176
	ds_read_b128 v[192:195], v154 offset:51200
	ds_read_b128 v[196:199], v154 offset:52224
	ds_read_b128 v[200:203], v154 offset:53248
	ds_read_b128 v[204:207], v154 offset:54272
	ds_read_b128 v[208:211], v154 offset:55296
	ds_read_b128 v[212:215], v154 offset:56320
	global_load_lds_dwordx4 v[216:217], off
	s_add_i32 m0, s26, 0x2000
	s_add_u32 s24, s24, 0x80080
	v_lshl_add_u64 v[216:217], v[218:219], 0, s[8:9]
	s_addc_u32 s25, s25, 0
	s_add_i32 s26, s71, s33
	global_load_lds_dwordx4 v[216:217], off
	s_mov_b32 m0, s26
	s_nop 0
	global_load_lds_dwordx4 v134, s[24:25]
	s_add_i32 m0, s26, 0x2000
	s_nop 0
	global_load_lds_dwordx4 v130, s[24:25]
	v_lshl_add_u64 v[216:217], v[220:221], 0, s[8:9]
	s_mov_b32 m0, s44
	s_nop 0
	global_load_lds_dwordx4 v[216:217], off
	v_lshl_add_u64 v[216:217], v[222:223], 0, s[8:9]
	s_mov_b32 m0, s45
	s_nop 0
	global_load_lds_dwordx4 v[216:217], off
	s_waitcnt vmcnt(8)
	s_waitcnt lgkmcnt(0)
	s_barrier
	s_setprio 1
	s_waitcnt lgkmcnt(0)
	v_mfma_f32_16x16x32_bf16 v[62:65], v[146:149], v[184:187], v[62:65]
	v_mfma_f32_16x16x32_bf16 v[58:61], v[160:163], v[184:187], v[58:61]
	v_mfma_f32_16x16x32_bf16 v[46:49], v[146:149], v[192:195], v[46:49]
	v_mfma_f32_16x16x32_bf16 v[42:45], v[160:163], v[192:195], v[42:45]
	v_mfma_f32_16x16x32_bf16 v[30:33], v[146:149], v[200:203], v[30:33]
	v_mfma_f32_16x16x32_bf16 v[26:29], v[160:163], v[200:203], v[26:29]
	v_mfma_f32_16x16x32_bf16 v[14:17], v[146:149], v[208:211], v[14:17]
	v_mfma_f32_16x16x32_bf16 v[10:13], v[160:163], v[208:211], v[10:13]
	v_mfma_f32_16x16x32_bf16 v[62:65], v[156:159], v[188:191], v[62:65]
	v_mfma_f32_16x16x32_bf16 v[58:61], v[164:167], v[188:191], v[58:61]
	v_mfma_f32_16x16x32_bf16 v[46:49], v[156:159], v[196:199], v[46:49]
	v_mfma_f32_16x16x32_bf16 v[42:45], v[164:167], v[196:199], v[42:45]
	v_mfma_f32_16x16x32_bf16 v[30:33], v[156:159], v[204:207], v[30:33]
	v_mfma_f32_16x16x32_bf16 v[26:29], v[164:167], v[204:207], v[26:29]
	v_mfma_f32_16x16x32_bf16 v[14:17], v[156:159], v[212:215], v[14:17]
	v_mfma_f32_16x16x32_bf16 v[10:13], v[164:167], v[212:215], v[10:13]
	v_mfma_f32_16x16x32_bf16 v[54:57], v[168:171], v[184:187], v[54:57]
	v_mfma_f32_16x16x32_bf16 v[50:53], v[176:179], v[184:187], v[50:53]
	v_mfma_f32_16x16x32_bf16 v[38:41], v[168:171], v[192:195], v[38:41]
	v_mfma_f32_16x16x32_bf16 v[34:37], v[176:179], v[192:195], v[34:37]
	v_mfma_f32_16x16x32_bf16 v[22:25], v[168:171], v[200:203], v[22:25]
	v_mfma_f32_16x16x32_bf16 v[18:21], v[176:179], v[200:203], v[18:21]
	v_mfma_f32_16x16x32_bf16 v[6:9], v[168:171], v[208:211], v[6:9]
	v_mfma_f32_16x16x32_bf16 v[2:5], v[176:179], v[208:211], v[2:5]
	v_mfma_f32_16x16x32_bf16 v[54:57], v[172:175], v[188:191], v[54:57]
	v_mfma_f32_16x16x32_bf16 v[50:53], v[180:183], v[188:191], v[50:53]
	v_mfma_f32_16x16x32_bf16 v[38:41], v[172:175], v[196:199], v[38:41]
	v_mfma_f32_16x16x32_bf16 v[34:37], v[180:183], v[196:199], v[34:37]
	v_mfma_f32_16x16x32_bf16 v[22:25], v[172:175], v[204:207], v[22:25]
	v_mfma_f32_16x16x32_bf16 v[18:21], v[180:183], v[204:207], v[18:21]
	v_mfma_f32_16x16x32_bf16 v[6:9], v[172:175], v[212:215], v[6:9]
	v_mfma_f32_16x16x32_bf16 v[2:5], v[180:183], v[212:215], v[2:5]
	s_setprio 0
	s_barrier
	s_add_i32 s69, s69, 2
	s_add_u32 s22, s22, 0x100
	s_addc_u32 s23, s23, 0
	s_add_u32 s67, s67, 0x100
	s_addc_u32 s68, s68, 0
	s_cmp_gt_u32 s69, 29
	s_cbranch_scc0 .LBB0_574
	s_and_b64 vcc, exec, s[10:11]
	s_cbranch_vccz .LBB0_577
	s_barrier

.LBB0_659:
	ds_read_b128 v[150:153], v211
	ds_read_b128 v[154:157], v211 offset:1024
	ds_read_b128 v[158:161], v211 offset:2048
	ds_read_b128 v[162:165], v211 offset:3072
	ds_read_b128 v[166:169], v212
	ds_read_b128 v[170:173], v212 offset:1024
	ds_read_b128 v[174:177], v212 offset:2048
	ds_read_b128 v[178:181], v212 offset:3072
	s_add_u32 s36, s0, 0xffea8080
	s_addc_u32 s37, s1, -1
	s_cmpk_eq_i32 s44, 0x52
	s_cselect_b32 s43, s27, s37
	s_cselect_b32 s42, s26, s36
	s_cselect_b32 s37, s29, s35
	s_cselect_b32 s36, s28, s31
	s_add_i32 m0, s63, 0xc000
	ds_read_b128 v[182:185], v213
	ds_read_b128 v[186:189], v213 offset:1024
	ds_read_b128 v[190:193], v213 offset:2048
	ds_read_b128 v[194:197], v213 offset:3072
	ds_read_b128 v[198:201], v213 offset:4096
	ds_read_b128 v[202:205], v213 offset:5120
	ds_read_b128 v[218:221], v213 offset:6144
	ds_read_b128 v[222:225], v213 offset:7168
	global_load_lds_dwordx4 v142, s[0:1]
	s_add_i32 m0, s63, 0xe000
	s_nop 0
	global_load_lds_dwordx4 v144, s[0:1]
	s_waitcnt vmcnt(8)
	s_waitcnt lgkmcnt(0)
	s_barrier
	s_setprio 1
	s_waitcnt lgkmcnt(0)
	v_mfma_f32_16x16x32_bf16 v[126:129], v[150:153], v[182:185], v[126:129]
	v_mfma_f32_16x16x32_bf16 v[122:125], v[158:161], v[182:185], v[122:125]
	v_mfma_f32_16x16x32_bf16 v[110:113], v[150:153], v[190:193], v[110:113]
	v_mfma_f32_16x16x32_bf16 v[106:109], v[158:161], v[190:193], v[106:109]
	v_mfma_f32_16x16x32_bf16 v[94:97], v[150:153], v[198:201], v[94:97]
	v_mfma_f32_16x16x32_bf16 v[90:93], v[158:161], v[198:201], v[90:93]
	v_mfma_f32_16x16x32_bf16 v[78:81], v[150:153], v[218:221], v[78:81]
	v_mfma_f32_16x16x32_bf16 v[74:77], v[158:161], v[218:221], v[74:77]
	v_mfma_f32_16x16x32_bf16 v[126:129], v[154:157], v[186:189], v[126:129]
	v_mfma_f32_16x16x32_bf16 v[122:125], v[162:165], v[186:189], v[122:125]
	v_mfma_f32_16x16x32_bf16 v[110:113], v[154:157], v[194:197], v[110:113]
	v_mfma_f32_16x16x32_bf16 v[106:109], v[162:165], v[194:197], v[106:109]
	v_mfma_f32_16x16x32_bf16 v[94:97], v[154:157], v[202:205], v[94:97]
	v_mfma_f32_16x16x32_bf16 v[90:93], v[162:165], v[202:205], v[90:93]
	v_mfma_f32_16x16x32_bf16 v[78:81], v[154:157], v[222:225], v[78:81]
	v_mfma_f32_16x16x32_bf16 v[74:77], v[162:165], v[222:225], v[74:77]
	v_mfma_f32_16x16x32_bf16 v[118:121], v[166:169], v[182:185], v[118:121]
	v_mfma_f32_16x16x32_bf16 v[114:117], v[174:177], v[182:185], v[114:117]
	v_mfma_f32_16x16x32_bf16 v[102:105], v[166:169], v[190:193], v[102:105]
	v_mfma_f32_16x16x32_bf16 v[98:101], v[174:177], v[190:193], v[98:101]
	v_mfma_f32_16x16x32_bf16 v[86:89], v[166:169], v[198:201], v[86:89]
	v_mfma_f32_16x16x32_bf16 v[82:85], v[174:177], v[198:201], v[82:85]
	v_mfma_f32_16x16x32_bf16 v[70:73], v[166:169], v[218:221], v[70:73]
	v_mfma_f32_16x16x32_bf16 v[66:69], v[174:177], v[218:221], v[66:69]
	v_mfma_f32_16x16x32_bf16 v[118:121], v[170:173], v[186:189], v[118:121]
	v_mfma_f32_16x16x32_bf16 v[114:117], v[178:181], v[186:189], v[114:117]
	v_mfma_f32_16x16x32_bf16 v[102:105], v[170:173], v[194:197], v[102:105]
	v_mfma_f32_16x16x32_bf16 v[98:101], v[178:181], v[194:197], v[98:101]
	v_mfma_f32_16x16x32_bf16 v[86:89], v[170:173], v[202:205], v[86:89]
	v_mfma_f32_16x16x32_bf16 v[82:85], v[178:181], v[202:205], v[82:85]
	v_mfma_f32_16x16x32_bf16 v[70:73], v[170:173], v[222:225], v[70:73]
	v_mfma_f32_16x16x32_bf16 v[66:69], v[178:181], v[222:225], v[66:69]
	s_setprio 0
	s_barrier
	s_add_i32 s45, s75, s62
	v_lshl_add_u64 v[226:227], s[36:37], 0, v[132:133]
	s_mov_b32 m0, s45
	ds_read_b128 v[182:185], v213 offset:16384
	ds_read_b128 v[186:189], v213 offset:17408
	ds_read_b128 v[190:193], v213 offset:18432
	ds_read_b128 v[194:197], v213 offset:19456
	ds_read_b128 v[198:201], v213 offset:20480
	ds_read_b128 v[202:205], v213 offset:21504
	ds_read_b128 v[218:221], v213 offset:22528
	ds_read_b128 v[222:225], v213 offset:23552
	global_load_lds_dwordx4 v132, s[36:37]
	s_add_i32 m0, s45, 0x2000
	s_add_u32 s82, s36, 0x158000
	v_lshl_add_u64 v[228:229], s[36:37], 0, v[136:137]
	s_addc_u32 s83, s37, 0
	s_add_i32 s45, s76, s62
	global_load_lds_dwordx4 v136, s[36:37]
	s_mov_b32 m0, s45
	v_lshl_add_u64 v[232:233], s[42:43], 0, v[134:135]
	global_load_lds_dwordx4 v132, s[82:83]
	s_add_i32 m0, s45, 0x2000
	s_nop 0
	global_load_lds_dwordx4 v136, s[82:83]
	v_lshl_add_u64 v[230:231], s[42:43], 0, v[130:131]
	s_mov_b32 m0, s63
	s_nop 0
	global_load_lds_dwordx4 v130, s[42:43]
	s_mov_b32 m0, s64
	s_nop 0
	global_load_lds_dwordx4 v134, s[42:43]
	s_waitcnt vmcnt(8)
	s_waitcnt lgkmcnt(0)
	s_barrier
	s_setprio 1
	s_waitcnt lgkmcnt(0)
	v_mfma_f32_16x16x32_bf16 v[62:65], v[150:153], v[182:185], v[62:65]
	v_mfma_f32_16x16x32_bf16 v[58:61], v[158:161], v[182:185], v[58:61]
	v_mfma_f32_16x16x32_bf16 v[46:49], v[150:153], v[190:193], v[46:49]
	v_mfma_f32_16x16x32_bf16 v[42:45], v[158:161], v[190:193], v[42:45]
	v_mfma_f32_16x16x32_bf16 v[30:33], v[150:153], v[198:201], v[30:33]
	v_mfma_f32_16x16x32_bf16 v[26:29], v[158:161], v[198:201], v[26:29]
	v_mfma_f32_16x16x32_bf16 v[14:17], v[150:153], v[218:221], v[14:17]
	v_mfma_f32_16x16x32_bf16 v[10:13], v[158:161], v[218:221], v[10:13]
	v_mfma_f32_16x16x32_bf16 v[62:65], v[154:157], v[186:189], v[62:65]
	v_mfma_f32_16x16x32_bf16 v[58:61], v[162:165], v[186:189], v[58:61]
	v_mfma_f32_16x16x32_bf16 v[46:49], v[154:157], v[194:197], v[46:49]
	v_mfma_f32_16x16x32_bf16 v[42:45], v[162:165], v[194:197], v[42:45]
	v_mfma_f32_16x16x32_bf16 v[30:33], v[154:157], v[202:205], v[30:33]
	v_mfma_f32_16x16x32_bf16 v[26:29], v[162:165], v[202:205], v[26:29]
	v_mfma_f32_16x16x32_bf16 v[14:17], v[154:157], v[222:225], v[14:17]
	v_mfma_f32_16x16x32_bf16 v[10:13], v[162:165], v[222:225], v[10:13]
	v_mfma_f32_16x16x32_bf16 v[54:57], v[166:169], v[182:185], v[54:57]
	v_mfma_f32_16x16x32_bf16 v[50:53], v[174:177], v[182:185], v[50:53]
	v_mfma_f32_16x16x32_bf16 v[38:41], v[166:169], v[190:193], v[38:41]
	v_mfma_f32_16x16x32_bf16 v[34:37], v[174:177], v[190:193], v[34:37]
	v_mfma_f32_16x16x32_bf16 v[22:25], v[166:169], v[198:201], v[22:25]
	v_mfma_f32_16x16x32_bf16 v[18:21], v[174:177], v[198:201], v[18:21]
	v_mfma_f32_16x16x32_bf16 v[6:9], v[166:169], v[218:221], v[6:9]
	v_mfma_f32_16x16x32_bf16 v[2:5], v[174:177], v[218:221], v[2:5]
	v_mfma_f32_16x16x32_bf16 v[54:57], v[170:173], v[186:189], v[54:57]
	v_mfma_f32_16x16x32_bf16 v[50:53], v[178:181], v[186:189], v[50:53]
	v_mfma_f32_16x16x32_bf16 v[38:41], v[170:173], v[194:197], v[38:41]
	v_mfma_f32_16x16x32_bf16 v[34:37], v[178:181], v[194:197], v[34:37]
	v_mfma_f32_16x16x32_bf16 v[22:25], v[170:173], v[202:205], v[22:25]
	v_mfma_f32_16x16x32_bf16 v[18:21], v[178:181], v[202:205], v[18:21]
	v_mfma_f32_16x16x32_bf16 v[6:9], v[170:173], v[222:225], v[6:9]
	v_mfma_f32_16x16x32_bf16 v[2:5], v[178:181], v[222:225], v[2:5]
	s_setprio 0
	s_barrier
	s_add_i32 s45, 0, 0x18000
	v_add_u32_e32 v139, s45, v206
	s_add_i32 s81, 0, 0x1c000
	ds_read_b128 v[150:153], v139
	ds_read_b128 v[154:157], v139 offset:1024
	ds_read_b128 v[158:161], v139 offset:2048
	ds_read_b128 v[162:165], v139 offset:3072
	v_add_u32_e32 v139, s81, v206
	ds_read_b128 v[166:169], v139
	ds_read_b128 v[170:173], v139 offset:1024
	ds_read_b128 v[174:177], v139 offset:2048
	ds_read_b128 v[178:181], v139 offset:3072
	s_add_u32 s42, s42, 0x158000
	s_addc_u32 s43, s43, 0
	s_mov_b32 m0, s65
	ds_read_b128 v[182:185], v213 offset:32768
	ds_read_b128 v[186:189], v213 offset:33792
	ds_read_b128 v[190:193], v213 offset:34816
	ds_read_b128 v[194:197], v213 offset:35840
	ds_read_b128 v[198:201], v213 offset:36864
	ds_read_b128 v[202:205], v213 offset:37888
	ds_read_b128 v[218:221], v213 offset:38912
	ds_read_b128 v[222:225], v213 offset:39936
	global_load_lds_dwordx4 v130, s[42:43]
	s_mov_b32 m0, s66
	s_nop 0
	global_load_lds_dwordx4 v134, s[42:43]
	s_waitcnt vmcnt(8)
	s_waitcnt lgkmcnt(0)
	s_barrier
	s_setprio 1
	s_waitcnt lgkmcnt(0)
	v_mfma_f32_16x16x32_bf16 v[126:129], v[150:153], v[182:185], v[126:129]
	v_mfma_f32_16x16x32_bf16 v[122:125], v[158:161], v[182:185], v[122:125]
	v_mfma_f32_16x16x32_bf16 v[110:113], v[150:153], v[190:193], v[110:113]
	v_mfma_f32_16x16x32_bf16 v[106:109], v[158:161], v[190:193], v[106:109]
	v_mfma_f32_16x16x32_bf16 v[94:97], v[150:153], v[198:201], v[94:97]
	v_mfma_f32_16x16x32_bf16 v[90:93], v[158:161], v[198:201], v[90:93]
	v_mfma_f32_16x16x32_bf16 v[78:81], v[150:153], v[218:221], v[78:81]
	v_mfma_f32_16x16x32_bf16 v[74:77], v[158:161], v[218:221], v[74:77]
	v_mfma_f32_16x16x32_bf16 v[126:129], v[154:157], v[186:189], v[126:129]
	v_mfma_f32_16x16x32_bf16 v[122:125], v[162:165], v[186:189], v[122:125]
	v_mfma_f32_16x16x32_bf16 v[110:113], v[154:157], v[194:197], v[110:113]
	v_mfma_f32_16x16x32_bf16 v[106:109], v[162:165], v[194:197], v[106:109]
	v_mfma_f32_16x16x32_bf16 v[94:97], v[154:157], v[202:205], v[94:97]
	v_mfma_f32_16x16x32_bf16 v[90:93], v[162:165], v[202:205], v[90:93]
	v_mfma_f32_16x16x32_bf16 v[78:81], v[154:157], v[222:225], v[78:81]
	v_mfma_f32_16x16x32_bf16 v[74:77], v[162:165], v[222:225], v[74:77]
	v_mfma_f32_16x16x32_bf16 v[118:121], v[166:169], v[182:185], v[118:121]
	v_mfma_f32_16x16x32_bf16 v[114:117], v[174:177], v[182:185], v[114:117]
	v_mfma_f32_16x16x32_bf16 v[102:105], v[166:169], v[190:193], v[102:105]
	v_mfma_f32_16x16x32_bf16 v[98:101], v[174:177], v[190:193], v[98:101]
	v_mfma_f32_16x16x32_bf16 v[86:89], v[166:169], v[198:201], v[86:89]
	v_mfma_f32_16x16x32_bf16 v[82:85], v[174:177], v[198:201], v[82:85]
	v_mfma_f32_16x16x32_bf16 v[70:73], v[166:169], v[218:221], v[70:73]
	v_mfma_f32_16x16x32_bf16 v[66:69], v[174:177], v[218:221], v[66:69]
	v_mfma_f32_16x16x32_bf16 v[118:121], v[170:173], v[186:189], v[118:121]
	v_mfma_f32_16x16x32_bf16 v[114:117], v[178:181], v[186:189], v[114:117]
	v_mfma_f32_16x16x32_bf16 v[102:105], v[170:173], v[194:197], v[102:105]
	v_mfma_f32_16x16x32_bf16 v[98:101], v[178:181], v[194:197], v[98:101]
	v_mfma_f32_16x16x32_bf16 v[86:89], v[170:173], v[202:205], v[86:89]
	v_mfma_f32_16x16x32_bf16 v[82:85], v[178:181], v[202:205], v[82:85]
	v_mfma_f32_16x16x32_bf16 v[70:73], v[170:173], v[222:225], v[70:73]
	v_mfma_f32_16x16x32_bf16 v[66:69], v[178:181], v[222:225], v[66:69]
	s_setprio 0
	s_barrier
	s_add_i32 s42, s45, s62
	v_lshl_add_u64 v[226:227], v[226:227], 0, s[20:21]
	s_mov_b32 m0, s42
	ds_read_b128 v[182:185], v213 offset:49152
	ds_read_b128 v[186:189], v213 offset:50176
	ds_read_b128 v[190:193], v213 offset:51200
	ds_read_b128 v[194:197], v213 offset:52224
	ds_read_b128 v[198:201], v213 offset:53248
	ds_read_b128 v[202:205], v213 offset:54272
	ds_read_b128 v[218:221], v213 offset:55296
	ds_read_b128 v[222:225], v213 offset:56320
	global_load_lds_dwordx4 v[226:227], off
	s_add_i32 m0, s42, 0x2000
	s_add_u32 s36, s36, 0x158080
	v_lshl_add_u64 v[226:227], v[228:229], 0, s[20:21]
	s_addc_u32 s37, s37, 0
	s_add_i32 s42, s81, s62
	global_load_lds_dwordx4 v[226:227], off
	s_mov_b32 m0, s42
	s_nop 0
	global_load_lds_dwordx4 v132, s[36:37]
	s_add_i32 m0, s42, 0x2000
	s_nop 0
	global_load_lds_dwordx4 v136, s[36:37]
	v_lshl_add_u64 v[226:227], v[230:231], 0, s[20:21]
	s_mov_b32 m0, s70
	s_nop 0
	global_load_lds_dwordx4 v[226:227], off
	v_lshl_add_u64 v[226:227], v[232:233], 0, s[20:21]
	s_mov_b32 m0, s71
	s_nop 0
	global_load_lds_dwordx4 v[226:227], off
	s_waitcnt vmcnt(8)
	s_waitcnt lgkmcnt(0)
	s_barrier
	s_setprio 1
	s_waitcnt lgkmcnt(0)
	v_mfma_f32_16x16x32_bf16 v[62:65], v[150:153], v[182:185], v[62:65]
	v_mfma_f32_16x16x32_bf16 v[58:61], v[158:161], v[182:185], v[58:61]
	v_mfma_f32_16x16x32_bf16 v[46:49], v[150:153], v[190:193], v[46:49]
	v_mfma_f32_16x16x32_bf16 v[42:45], v[158:161], v[190:193], v[42:45]
	v_mfma_f32_16x16x32_bf16 v[30:33], v[150:153], v[198:201], v[30:33]
	v_mfma_f32_16x16x32_bf16 v[26:29], v[158:161], v[198:201], v[26:29]
	v_mfma_f32_16x16x32_bf16 v[14:17], v[150:153], v[218:221], v[14:17]
	v_mfma_f32_16x16x32_bf16 v[10:13], v[158:161], v[218:221], v[10:13]
	v_mfma_f32_16x16x32_bf16 v[62:65], v[154:157], v[186:189], v[62:65]
	v_mfma_f32_16x16x32_bf16 v[58:61], v[162:165], v[186:189], v[58:61]
	v_mfma_f32_16x16x32_bf16 v[46:49], v[154:157], v[194:197], v[46:49]
	v_mfma_f32_16x16x32_bf16 v[42:45], v[162:165], v[194:197], v[42:45]
	v_mfma_f32_16x16x32_bf16 v[30:33], v[154:157], v[202:205], v[30:33]
	v_mfma_f32_16x16x32_bf16 v[26:29], v[162:165], v[202:205], v[26:29]
	v_mfma_f32_16x16x32_bf16 v[14:17], v[154:157], v[222:225], v[14:17]
	v_mfma_f32_16x16x32_bf16 v[10:13], v[162:165], v[222:225], v[10:13]
	v_mfma_f32_16x16x32_bf16 v[54:57], v[166:169], v[182:185], v[54:57]
	v_mfma_f32_16x16x32_bf16 v[50:53], v[174:177], v[182:185], v[50:53]
	v_mfma_f32_16x16x32_bf16 v[38:41], v[166:169], v[190:193], v[38:41]
	v_mfma_f32_16x16x32_bf16 v[34:37], v[174:177], v[190:193], v[34:37]
	v_mfma_f32_16x16x32_bf16 v[22:25], v[166:169], v[198:201], v[22:25]
	v_mfma_f32_16x16x32_bf16 v[18:21], v[174:177], v[198:201], v[18:21]
	v_mfma_f32_16x16x32_bf16 v[6:9], v[166:169], v[218:221], v[6:9]
	v_mfma_f32_16x16x32_bf16 v[2:5], v[174:177], v[218:221], v[2:5]
	v_mfma_f32_16x16x32_bf16 v[54:57], v[170:173], v[186:189], v[54:57]
	v_mfma_f32_16x16x32_bf16 v[50:53], v[178:181], v[186:189], v[50:53]
	v_mfma_f32_16x16x32_bf16 v[38:41], v[170:173], v[194:197], v[38:41]
	v_mfma_f32_16x16x32_bf16 v[34:37], v[178:181], v[194:197], v[34:37]
	v_mfma_f32_16x16x32_bf16 v[22:25], v[170:173], v[202:205], v[22:25]
	v_mfma_f32_16x16x32_bf16 v[18:21], v[178:181], v[202:205], v[18:21]
	v_mfma_f32_16x16x32_bf16 v[6:9], v[170:173], v[222:225], v[6:9]
	v_mfma_f32_16x16x32_bf16 v[2:5], v[178:181], v[222:225], v[2:5]
	s_setprio 0
	s_barrier
	s_add_i32 s44, s44, 2
	s_add_u32 s0, s0, 0x100
	s_addc_u32 s1, s1, 0
	s_add_u32 s31, s31, 0x100
	s_addc_u32 s35, s35, 0
	s_cmpk_gt_u32 s44, 0x53
	s_cbranch_scc0 .LBB0_659
	s_and_b64 vcc, exec, s[22:23]
	s_cbranch_vccz .LBB0_662
	s_barrier

.LBB0_767:
	ds_read_b128 v[146:149], v152
	ds_read_b128 v[156:159], v152 offset:1024
	ds_read_b128 v[160:163], v152 offset:2048
	ds_read_b128 v[164:167], v152 offset:3072
	ds_read_b128 v[168:171], v153
	ds_read_b128 v[172:175], v153 offset:1024
	ds_read_b128 v[176:179], v153 offset:2048
	ds_read_b128 v[180:183], v153 offset:3072
	s_add_u32 s24, s22, 0xfff80080
	s_addc_u32 s25, s23, -1
	s_cmp_eq_u32 s69, 28
	s_cselect_b32 s27, s15, s25
	s_cselect_b32 s26, s65, s24
	s_cselect_b32 s25, s13, s68
	s_cselect_b32 s24, s66, s67
	s_add_i32 m0, s21, 0xc000
	ds_read_b128 v[184:187], v154
	ds_read_b128 v[188:191], v154 offset:1024
	ds_read_b128 v[192:195], v154 offset:2048
	ds_read_b128 v[196:199], v154 offset:3072
	ds_read_b128 v[200:203], v154 offset:4096
	ds_read_b128 v[204:207], v154 offset:5120
	ds_read_b128 v[208:211], v154 offset:6144
	ds_read_b128 v[212:215], v154 offset:7168
	global_load_lds_dwordx4 v138, s[22:23]
	s_add_i32 m0, s21, 0xe000
	s_nop 0
	global_load_lds_dwordx4 v140, s[22:23]
	s_waitcnt vmcnt(8)
	s_waitcnt lgkmcnt(0)
	s_barrier
	s_setprio 1
	s_waitcnt lgkmcnt(0)
	v_mfma_f32_16x16x32_bf16 v[126:129], v[146:149], v[184:187], v[126:129]
	v_mfma_f32_16x16x32_bf16 v[122:125], v[160:163], v[184:187], v[122:125]
	v_mfma_f32_16x16x32_bf16 v[118:121], v[146:149], v[192:195], v[118:121]
	v_mfma_f32_16x16x32_bf16 v[110:113], v[160:163], v[192:195], v[110:113]
	v_mfma_f32_16x16x32_bf16 v[102:105], v[146:149], v[200:203], v[102:105]
	v_mfma_f32_16x16x32_bf16 v[94:97], v[160:163], v[200:203], v[94:97]
	v_mfma_f32_16x16x32_bf16 v[86:89], v[146:149], v[208:211], v[86:89]
	v_mfma_f32_16x16x32_bf16 v[78:81], v[160:163], v[208:211], v[78:81]
	v_mfma_f32_16x16x32_bf16 v[126:129], v[156:159], v[188:191], v[126:129]
	v_mfma_f32_16x16x32_bf16 v[122:125], v[164:167], v[188:191], v[122:125]
	v_mfma_f32_16x16x32_bf16 v[118:121], v[156:159], v[196:199], v[118:121]
	v_mfma_f32_16x16x32_bf16 v[110:113], v[164:167], v[196:199], v[110:113]
	v_mfma_f32_16x16x32_bf16 v[102:105], v[156:159], v[204:207], v[102:105]
	v_mfma_f32_16x16x32_bf16 v[94:97], v[164:167], v[204:207], v[94:97]
	v_mfma_f32_16x16x32_bf16 v[86:89], v[156:159], v[212:215], v[86:89]
	v_mfma_f32_16x16x32_bf16 v[78:81], v[164:167], v[212:215], v[78:81]
	v_mfma_f32_16x16x32_bf16 v[114:117], v[168:171], v[184:187], v[114:117]
	v_mfma_f32_16x16x32_bf16 v[106:109], v[176:179], v[184:187], v[106:109]
	v_mfma_f32_16x16x32_bf16 v[98:101], v[168:171], v[192:195], v[98:101]
	v_mfma_f32_16x16x32_bf16 v[90:93], v[176:179], v[192:195], v[90:93]
	v_mfma_f32_16x16x32_bf16 v[82:85], v[168:171], v[200:203], v[82:85]
	v_mfma_f32_16x16x32_bf16 v[74:77], v[176:179], v[200:203], v[74:77]
	v_mfma_f32_16x16x32_bf16 v[70:73], v[168:171], v[208:211], v[70:73]
	v_mfma_f32_16x16x32_bf16 v[66:69], v[176:179], v[208:211], v[66:69]
	v_mfma_f32_16x16x32_bf16 v[114:117], v[172:175], v[188:191], v[114:117]
	v_mfma_f32_16x16x32_bf16 v[106:109], v[180:183], v[188:191], v[106:109]
	v_mfma_f32_16x16x32_bf16 v[98:101], v[172:175], v[196:199], v[98:101]
	v_mfma_f32_16x16x32_bf16 v[90:93], v[180:183], v[196:199], v[90:93]
	v_mfma_f32_16x16x32_bf16 v[82:85], v[172:175], v[204:207], v[82:85]
	v_mfma_f32_16x16x32_bf16 v[74:77], v[180:183], v[204:207], v[74:77]
	v_mfma_f32_16x16x32_bf16 v[70:73], v[172:175], v[212:215], v[70:73]
	v_mfma_f32_16x16x32_bf16 v[66:69], v[180:183], v[212:215], v[66:69]
	s_setprio 0
	s_barrier
	s_add_i32 s70, s61, s33
	v_lshl_add_u64 v[216:217], s[24:25], 0, v[134:135]
	s_mov_b32 m0, s70
	ds_read_b128 v[184:187], v154 offset:16384
	ds_read_b128 v[188:191], v154 offset:17408
	ds_read_b128 v[192:195], v154 offset:18432
	ds_read_b128 v[196:199], v154 offset:19456
	ds_read_b128 v[200:203], v154 offset:20480
	ds_read_b128 v[204:207], v154 offset:21504
	ds_read_b128 v[208:211], v154 offset:22528
	ds_read_b128 v[212:215], v154 offset:23552
	global_load_lds_dwordx4 v134, s[24:25]
	s_add_i32 m0, s70, 0x2000
	s_add_u32 s70, s24, 0x80000
	v_lshl_add_u64 v[218:219], s[24:25], 0, v[130:131]
	s_addc_u32 s71, s25, 0
	s_add_i32 s72, s62, s33
	global_load_lds_dwordx4 v130, s[24:25]
	s_mov_b32 m0, s72
	v_lshl_add_u64 v[222:223], s[26:27], 0, v[132:133]
	global_load_lds_dwordx4 v134, s[70:71]
	s_add_i32 m0, s72, 0x2000
	s_nop 0
	global_load_lds_dwordx4 v130, s[70:71]
	v_lshl_add_u64 v[220:221], s[26:27], 0, v[136:137]
	s_mov_b32 m0, s21
	s_nop 0
	global_load_lds_dwordx4 v136, s[26:27]
	s_mov_b32 m0, s36
	s_nop 0
	global_load_lds_dwordx4 v132, s[26:27]
	s_waitcnt vmcnt(8)
	s_waitcnt lgkmcnt(0)
	s_barrier
	s_setprio 1
	s_waitcnt lgkmcnt(0)
	v_mfma_f32_16x16x32_bf16 v[62:65], v[146:149], v[184:187], v[62:65]
	v_mfma_f32_16x16x32_bf16 v[58:61], v[160:163], v[184:187], v[58:61]
	v_mfma_f32_16x16x32_bf16 v[54:57], v[146:149], v[192:195], v[54:57]
	v_mfma_f32_16x16x32_bf16 v[46:49], v[160:163], v[192:195], v[46:49]
	v_mfma_f32_16x16x32_bf16 v[38:41], v[146:149], v[200:203], v[38:41]
	v_mfma_f32_16x16x32_bf16 v[30:33], v[160:163], v[200:203], v[30:33]
	v_mfma_f32_16x16x32_bf16 v[22:25], v[146:149], v[208:211], v[22:25]
	v_mfma_f32_16x16x32_bf16 v[14:17], v[160:163], v[208:211], v[14:17]
	v_mfma_f32_16x16x32_bf16 v[62:65], v[156:159], v[188:191], v[62:65]
	v_mfma_f32_16x16x32_bf16 v[58:61], v[164:167], v[188:191], v[58:61]
	v_mfma_f32_16x16x32_bf16 v[54:57], v[156:159], v[196:199], v[54:57]
	v_mfma_f32_16x16x32_bf16 v[46:49], v[164:167], v[196:199], v[46:49]
	v_mfma_f32_16x16x32_bf16 v[38:41], v[156:159], v[204:207], v[38:41]
	v_mfma_f32_16x16x32_bf16 v[30:33], v[164:167], v[204:207], v[30:33]
	v_mfma_f32_16x16x32_bf16 v[22:25], v[156:159], v[212:215], v[22:25]
	v_mfma_f32_16x16x32_bf16 v[14:17], v[164:167], v[212:215], v[14:17]
	v_mfma_f32_16x16x32_bf16 v[50:53], v[168:171], v[184:187], v[50:53]
	v_mfma_f32_16x16x32_bf16 v[42:45], v[176:179], v[184:187], v[42:45]
	v_mfma_f32_16x16x32_bf16 v[34:37], v[168:171], v[192:195], v[34:37]
	v_mfma_f32_16x16x32_bf16 v[26:29], v[176:179], v[192:195], v[26:29]
	v_mfma_f32_16x16x32_bf16 v[18:21], v[168:171], v[200:203], v[18:21]
	v_mfma_f32_16x16x32_bf16 v[10:13], v[176:179], v[200:203], v[10:13]
	v_mfma_f32_16x16x32_bf16 v[6:9], v[168:171], v[208:211], v[6:9]
	v_mfma_f32_16x16x32_bf16 v[2:5], v[176:179], v[208:211], v[2:5]
	v_mfma_f32_16x16x32_bf16 v[50:53], v[172:175], v[188:191], v[50:53]
	v_mfma_f32_16x16x32_bf16 v[42:45], v[180:183], v[188:191], v[42:45]
	v_mfma_f32_16x16x32_bf16 v[34:37], v[172:175], v[196:199], v[34:37]
	v_mfma_f32_16x16x32_bf16 v[26:29], v[180:183], v[196:199], v[26:29]
	v_mfma_f32_16x16x32_bf16 v[18:21], v[172:175], v[204:207], v[18:21]
	v_mfma_f32_16x16x32_bf16 v[10:13], v[180:183], v[204:207], v[10:13]
	v_mfma_f32_16x16x32_bf16 v[6:9], v[172:175], v[212:215], v[6:9]
	v_mfma_f32_16x16x32_bf16 v[2:5], v[180:183], v[212:215], v[2:5]
	s_setprio 0
	s_barrier
	s_add_i32 s70, 0, 0x18000
	v_add_u32_e32 v155, s70, v150
	s_add_i32 s71, 0, 0x1c000
	ds_read_b128 v[146:149], v155
	ds_read_b128 v[156:159], v155 offset:1024
	ds_read_b128 v[160:163], v155 offset:2048
	ds_read_b128 v[164:167], v155 offset:3072
	v_add_u32_e32 v155, s71, v150
	ds_read_b128 v[168:171], v155
	ds_read_b128 v[172:175], v155 offset:1024
	ds_read_b128 v[176:179], v155 offset:2048
	ds_read_b128 v[180:183], v155 offset:3072
	s_add_u32 s26, s26, 0x80000
	s_addc_u32 s27, s27, 0
	s_mov_b32 m0, s37
	ds_read_b128 v[184:187], v154 offset:32768
	ds_read_b128 v[188:191], v154 offset:33792
	ds_read_b128 v[192:195], v154 offset:34816
	ds_read_b128 v[196:199], v154 offset:35840
	ds_read_b128 v[200:203], v154 offset:36864
	ds_read_b128 v[204:207], v154 offset:37888
	ds_read_b128 v[208:211], v154 offset:38912
	ds_read_b128 v[212:215], v154 offset:39936
	global_load_lds_dwordx4 v136, s[26:27]
	s_mov_b32 m0, s42
	s_nop 0
	global_load_lds_dwordx4 v132, s[26:27]
	s_waitcnt vmcnt(8)
	s_waitcnt lgkmcnt(0)
	s_barrier
	s_setprio 1
	s_waitcnt lgkmcnt(0)
	v_mfma_f32_16x16x32_bf16 v[126:129], v[146:149], v[184:187], v[126:129]
	v_mfma_f32_16x16x32_bf16 v[122:125], v[160:163], v[184:187], v[122:125]
	v_mfma_f32_16x16x32_bf16 v[118:121], v[146:149], v[192:195], v[118:121]
	v_mfma_f32_16x16x32_bf16 v[110:113], v[160:163], v[192:195], v[110:113]
	v_mfma_f32_16x16x32_bf16 v[102:105], v[146:149], v[200:203], v[102:105]
	v_mfma_f32_16x16x32_bf16 v[94:97], v[160:163], v[200:203], v[94:97]
	v_mfma_f32_16x16x32_bf16 v[86:89], v[146:149], v[208:211], v[86:89]
	v_mfma_f32_16x16x32_bf16 v[78:81], v[160:163], v[208:211], v[78:81]
	v_mfma_f32_16x16x32_bf16 v[126:129], v[156:159], v[188:191], v[126:129]
	v_mfma_f32_16x16x32_bf16 v[122:125], v[164:167], v[188:191], v[122:125]
	v_mfma_f32_16x16x32_bf16 v[118:121], v[156:159], v[196:199], v[118:121]
	v_mfma_f32_16x16x32_bf16 v[110:113], v[164:167], v[196:199], v[110:113]
	v_mfma_f32_16x16x32_bf16 v[102:105], v[156:159], v[204:207], v[102:105]
	v_mfma_f32_16x16x32_bf16 v[94:97], v[164:167], v[204:207], v[94:97]
	v_mfma_f32_16x16x32_bf16 v[86:89], v[156:159], v[212:215], v[86:89]
	v_mfma_f32_16x16x32_bf16 v[78:81], v[164:167], v[212:215], v[78:81]
	v_mfma_f32_16x16x32_bf16 v[114:117], v[168:171], v[184:187], v[114:117]
	v_mfma_f32_16x16x32_bf16 v[106:109], v[176:179], v[184:187], v[106:109]
	v_mfma_f32_16x16x32_bf16 v[98:101], v[168:171], v[192:195], v[98:101]
	v_mfma_f32_16x16x32_bf16 v[90:93], v[176:179], v[192:195], v[90:93]
	v_mfma_f32_16x16x32_bf16 v[82:85], v[168:171], v[200:203], v[82:85]
	v_mfma_f32_16x16x32_bf16 v[74:77], v[176:179], v[200:203], v[74:77]
	v_mfma_f32_16x16x32_bf16 v[70:73], v[168:171], v[208:211], v[70:73]
	v_mfma_f32_16x16x32_bf16 v[66:69], v[176:179], v[208:211], v[66:69]
	v_mfma_f32_16x16x32_bf16 v[114:117], v[172:175], v[188:191], v[114:117]
	v_mfma_f32_16x16x32_bf16 v[106:109], v[180:183], v[188:191], v[106:109]
	v_mfma_f32_16x16x32_bf16 v[98:101], v[172:175], v[196:199], v[98:101]
	v_mfma_f32_16x16x32_bf16 v[90:93], v[180:183], v[196:199], v[90:93]
	v_mfma_f32_16x16x32_bf16 v[82:85], v[172:175], v[204:207], v[82:85]
	v_mfma_f32_16x16x32_bf16 v[74:77], v[180:183], v[204:207], v[74:77]
	v_mfma_f32_16x16x32_bf16 v[70:73], v[172:175], v[212:215], v[70:73]
	v_mfma_f32_16x16x32_bf16 v[66:69], v[180:183], v[212:215], v[66:69]
	s_setprio 0
	s_barrier
	s_add_i32 s26, s70, s33
	v_lshl_add_u64 v[216:217], v[216:217], 0, s[8:9]
	s_mov_b32 m0, s26
	ds_read_b128 v[184:187], v154 offset:49152
	ds_read_b128 v[188:191], v154 offset:50176
	ds_read_b128 v[192:195], v154 offset:51200
	ds_read_b128 v[196:199], v154 offset:52224
	ds_read_b128 v[200:203], v154 offset:53248
	ds_read_b128 v[204:207], v154 offset:54272
	ds_read_b128 v[208:211], v154 offset:55296
	ds_read_b128 v[212:215], v154 offset:56320
	global_load_lds_dwordx4 v[216:217], off
	s_add_i32 m0, s26, 0x2000
	s_add_u32 s24, s24, 0x80080
	v_lshl_add_u64 v[216:217], v[218:219], 0, s[8:9]
	s_addc_u32 s25, s25, 0
	s_add_i32 s26, s71, s33
	global_load_lds_dwordx4 v[216:217], off
	s_mov_b32 m0, s26
	s_nop 0
	global_load_lds_dwordx4 v134, s[24:25]
	s_add_i32 m0, s26, 0x2000
	s_nop 0
	global_load_lds_dwordx4 v130, s[24:25]
	v_lshl_add_u64 v[216:217], v[220:221], 0, s[8:9]
	s_mov_b32 m0, s44
	s_nop 0
	global_load_lds_dwordx4 v[216:217], off
	v_lshl_add_u64 v[216:217], v[222:223], 0, s[8:9]
	s_mov_b32 m0, s45
	s_nop 0
	global_load_lds_dwordx4 v[216:217], off
	s_waitcnt vmcnt(8)
	s_waitcnt lgkmcnt(0)
	s_barrier
	s_setprio 1
	s_waitcnt lgkmcnt(0)
	v_mfma_f32_16x16x32_bf16 v[62:65], v[146:149], v[184:187], v[62:65]
	v_mfma_f32_16x16x32_bf16 v[58:61], v[160:163], v[184:187], v[58:61]
	v_mfma_f32_16x16x32_bf16 v[54:57], v[146:149], v[192:195], v[54:57]
	v_mfma_f32_16x16x32_bf16 v[46:49], v[160:163], v[192:195], v[46:49]
	v_mfma_f32_16x16x32_bf16 v[38:41], v[146:149], v[200:203], v[38:41]
	v_mfma_f32_16x16x32_bf16 v[30:33], v[160:163], v[200:203], v[30:33]
	v_mfma_f32_16x16x32_bf16 v[22:25], v[146:149], v[208:211], v[22:25]
	v_mfma_f32_16x16x32_bf16 v[14:17], v[160:163], v[208:211], v[14:17]
	v_mfma_f32_16x16x32_bf16 v[62:65], v[156:159], v[188:191], v[62:65]
	v_mfma_f32_16x16x32_bf16 v[58:61], v[164:167], v[188:191], v[58:61]
	v_mfma_f32_16x16x32_bf16 v[54:57], v[156:159], v[196:199], v[54:57]
	v_mfma_f32_16x16x32_bf16 v[46:49], v[164:167], v[196:199], v[46:49]
	v_mfma_f32_16x16x32_bf16 v[38:41], v[156:159], v[204:207], v[38:41]
	v_mfma_f32_16x16x32_bf16 v[30:33], v[164:167], v[204:207], v[30:33]
	v_mfma_f32_16x16x32_bf16 v[22:25], v[156:159], v[212:215], v[22:25]
	v_mfma_f32_16x16x32_bf16 v[14:17], v[164:167], v[212:215], v[14:17]
	v_mfma_f32_16x16x32_bf16 v[50:53], v[168:171], v[184:187], v[50:53]
	v_mfma_f32_16x16x32_bf16 v[42:45], v[176:179], v[184:187], v[42:45]
	v_mfma_f32_16x16x32_bf16 v[34:37], v[168:171], v[192:195], v[34:37]
	v_mfma_f32_16x16x32_bf16 v[26:29], v[176:179], v[192:195], v[26:29]
	v_mfma_f32_16x16x32_bf16 v[18:21], v[168:171], v[200:203], v[18:21]
	v_mfma_f32_16x16x32_bf16 v[10:13], v[176:179], v[200:203], v[10:13]
	v_mfma_f32_16x16x32_bf16 v[6:9], v[168:171], v[208:211], v[6:9]
	v_mfma_f32_16x16x32_bf16 v[2:5], v[176:179], v[208:211], v[2:5]
	v_mfma_f32_16x16x32_bf16 v[50:53], v[172:175], v[188:191], v[50:53]
	v_mfma_f32_16x16x32_bf16 v[42:45], v[180:183], v[188:191], v[42:45]
	v_mfma_f32_16x16x32_bf16 v[34:37], v[172:175], v[196:199], v[34:37]
	v_mfma_f32_16x16x32_bf16 v[26:29], v[180:183], v[196:199], v[26:29]
	v_mfma_f32_16x16x32_bf16 v[18:21], v[172:175], v[204:207], v[18:21]
	v_mfma_f32_16x16x32_bf16 v[10:13], v[180:183], v[204:207], v[10:13]
	v_mfma_f32_16x16x32_bf16 v[6:9], v[172:175], v[212:215], v[6:9]
	v_mfma_f32_16x16x32_bf16 v[2:5], v[180:183], v[212:215], v[2:5]
	s_setprio 0
	s_barrier
	s_add_i32 s69, s69, 2
	s_add_u32 s22, s22, 0x100
	s_addc_u32 s23, s23, 0
	s_add_u32 s67, s67, 0x100
	s_addc_u32 s68, s68, 0
	s_cmp_gt_u32 s69, 29
	s_cbranch_scc0 .LBB0_767
	s_and_b64 vcc, exec, s[10:11]
	s_cbranch_vccz .LBB0_770
	s_barrier

.LBB0_1043:
	ds_read_b128 v[26:29], v209
	ds_read_b128 v[30:33], v209 offset:1024
	ds_read_b128 v[18:21], v209 offset:2048
	ds_read_b128 v[22:25], v209 offset:3072
	ds_read_b128 v[10:13], v210
	ds_read_b128 v[14:17], v210 offset:1024
	ds_read_b128 v[2:5], v210 offset:2048
	ds_read_b128 v[6:9], v210 offset:3072
	s_add_u32 s44, s40, 0xfffc0080
	s_addc_u32 s45, s41, -1
	s_cmp_eq_u32 s81, 12
	s_cselect_b32 s49, s1, s45
	s_cselect_b32 s48, s35, s44
	s_cselect_b32 s45, s31, s61
	s_cselect_b32 s44, s43, s60
	s_add_i32 m0, s65, 0xc000
	ds_read_b128 v[182:185], v211
	ds_read_b128 v[186:189], v211 offset:1024
	ds_read_b128 v[190:193], v211 offset:2048
	ds_read_b128 v[194:197], v211 offset:3072
	ds_read_b128 v[218:221], v211 offset:4096
	ds_read_b128 v[222:225], v211 offset:5120
	ds_read_b128 v[226:229], v211 offset:6144
	ds_read_b128 v[230:233], v211 offset:7168
	global_load_lds_dwordx4 v174, s[40:41]
	s_add_i32 m0, s65, 0xe000
	s_nop 0
	global_load_lds_dwordx4 v176, s[40:41]
	s_waitcnt vmcnt(8)
	s_waitcnt lgkmcnt(0)
	s_barrier
	s_setprio 1
	s_waitcnt lgkmcnt(0)
	v_mfma_scale_f32_16x16x128_f8f6f4 v[158:161], v[26:33], v[182:189], v[158:161], v212, v213 op_sel_hi:[0,0,0]
	v_mfma_scale_f32_16x16x128_f8f6f4 v[154:157], v[18:25], v[182:189], v[154:157], v212, v213 op_sel_hi:[0,0,0]
	v_mfma_scale_f32_16x16x128_f8f6f4 v[142:145], v[26:33], v[190:197], v[142:145], v212, v213 op_sel_hi:[0,0,0]
	v_mfma_scale_f32_16x16x128_f8f6f4 v[138:141], v[18:25], v[190:197], v[138:141], v212, v213 op_sel_hi:[0,0,0]
	v_mfma_scale_f32_16x16x128_f8f6f4 v[126:129], v[26:33], v[218:225], v[126:129], v212, v213 op_sel_hi:[0,0,0]
	v_mfma_scale_f32_16x16x128_f8f6f4 v[122:125], v[18:25], v[218:225], v[122:125], v212, v213 op_sel_hi:[0,0,0]
	v_mfma_scale_f32_16x16x128_f8f6f4 v[110:113], v[26:33], v[226:233], v[110:113], v212, v213 op_sel_hi:[0,0,0]
	v_mfma_scale_f32_16x16x128_f8f6f4 v[106:109], v[18:25], v[226:233], v[106:109], v212, v213 op_sel_hi:[0,0,0]
	v_mfma_scale_f32_16x16x128_f8f6f4 v[150:153], v[10:17], v[182:189], v[150:153], v212, v213 op_sel_hi:[0,0,0]
	v_mfma_scale_f32_16x16x128_f8f6f4 v[146:149], v[2:9], v[182:189], v[146:149], v212, v213 op_sel_hi:[0,0,0]
	v_mfma_scale_f32_16x16x128_f8f6f4 v[134:137], v[10:17], v[190:197], v[134:137], v212, v213 op_sel_hi:[0,0,0]
	v_mfma_scale_f32_16x16x128_f8f6f4 v[130:133], v[2:9], v[190:197], v[130:133], v212, v213 op_sel_hi:[0,0,0]
	v_mfma_scale_f32_16x16x128_f8f6f4 v[118:121], v[10:17], v[218:225], v[118:121], v212, v213 op_sel_hi:[0,0,0]
	v_mfma_scale_f32_16x16x128_f8f6f4 v[114:117], v[2:9], v[218:225], v[114:117], v212, v213 op_sel_hi:[0,0,0]
	v_mfma_scale_f32_16x16x128_f8f6f4 v[102:105], v[10:17], v[226:233], v[102:105], v212, v213 op_sel_hi:[0,0,0]
	v_mfma_scale_f32_16x16x128_f8f6f4 v[98:101], v[2:9], v[226:233], v[98:101], v212, v213 op_sel_hi:[0,0,0]
	s_setprio 0
	s_barrier
	s_add_i32 s82, s77, s64
	v_lshl_add_u64 v[182:183], s[44:45], 0, v[164:165]
	s_mov_b32 m0, s82
	ds_read_b128 v[190:193], v211 offset:16384
	ds_read_b128 v[194:197], v211 offset:17408
	ds_read_b128 v[218:221], v211 offset:18432
	ds_read_b128 v[222:225], v211 offset:19456
	ds_read_b128 v[226:229], v211 offset:20480
	ds_read_b128 v[230:233], v211 offset:21504
	ds_read_b128 v[234:237], v211 offset:22528
	ds_read_b128 v[238:241], v211 offset:23552
	global_load_lds_dwordx4 v164, s[44:45]
	s_add_i32 m0, s82, 0x2000
	s_add_u32 s82, s44, 0x40000
	v_lshl_add_u64 v[184:185], s[44:45], 0, v[168:169]
	s_addc_u32 s83, s45, 0
	s_add_i32 s84, s78, s64
	global_load_lds_dwordx4 v168, s[44:45]
	s_mov_b32 m0, s84
	v_lshl_add_u64 v[188:189], s[48:49], 0, v[166:167]
	global_load_lds_dwordx4 v164, s[82:83]
	s_add_i32 m0, s84, 0x2000
	s_nop 0
	global_load_lds_dwordx4 v168, s[82:83]
	v_lshl_add_u64 v[186:187], s[48:49], 0, v[162:163]
	s_mov_b32 m0, s65
	s_nop 0
	global_load_lds_dwordx4 v162, s[48:49]
	s_mov_b32 m0, s66
	s_nop 0
	global_load_lds_dwordx4 v166, s[48:49]
	s_waitcnt vmcnt(8)
	s_waitcnt lgkmcnt(0)
	s_barrier
	s_setprio 1
	s_waitcnt lgkmcnt(0)
	v_mfma_scale_f32_16x16x128_f8f6f4 v[94:97], v[26:33], v[190:197], v[94:97], v212, v213 op_sel_hi:[0,0,0]
	v_mfma_scale_f32_16x16x128_f8f6f4 v[90:93], v[18:25], v[190:197], v[90:93], v212, v213 op_sel_hi:[0,0,0]
	v_mfma_scale_f32_16x16x128_f8f6f4 v[78:81], v[26:33], v[218:225], v[78:81], v212, v213 op_sel_hi:[0,0,0]
	v_mfma_scale_f32_16x16x128_f8f6f4 v[74:77], v[18:25], v[218:225], v[74:77], v212, v213 op_sel_hi:[0,0,0]
	v_mfma_scale_f32_16x16x128_f8f6f4 v[62:65], v[26:33], v[226:233], v[62:65], v212, v213 op_sel_hi:[0,0,0]
	v_mfma_scale_f32_16x16x128_f8f6f4 v[58:61], v[18:25], v[226:233], v[58:61], v212, v213 op_sel_hi:[0,0,0]
	v_mfma_scale_f32_16x16x128_f8f6f4 v[46:49], v[26:33], v[234:241], v[46:49], v212, v213 op_sel_hi:[0,0,0]
	v_mfma_scale_f32_16x16x128_f8f6f4 v[42:45], v[18:25], v[234:241], v[42:45], v212, v213 op_sel_hi:[0,0,0]
	v_mfma_scale_f32_16x16x128_f8f6f4 v[86:89], v[10:17], v[190:197], v[86:89], v212, v213 op_sel_hi:[0,0,0]
	v_mfma_scale_f32_16x16x128_f8f6f4 v[82:85], v[2:9], v[190:197], v[82:85], v212, v213 op_sel_hi:[0,0,0]
	v_mfma_scale_f32_16x16x128_f8f6f4 v[70:73], v[10:17], v[218:225], v[70:73], v212, v213 op_sel_hi:[0,0,0]
	v_mfma_scale_f32_16x16x128_f8f6f4 v[66:69], v[2:9], v[218:225], v[66:69], v212, v213 op_sel_hi:[0,0,0]
	v_mfma_scale_f32_16x16x128_f8f6f4 v[54:57], v[10:17], v[226:233], v[54:57], v212, v213 op_sel_hi:[0,0,0]
	v_mfma_scale_f32_16x16x128_f8f6f4 v[50:53], v[2:9], v[226:233], v[50:53], v212, v213 op_sel_hi:[0,0,0]
	v_mfma_scale_f32_16x16x128_f8f6f4 v[38:41], v[10:17], v[234:241], v[38:41], v212, v213 op_sel_hi:[0,0,0]
	v_mfma_scale_f32_16x16x128_f8f6f4 v[34:37], v[2:9], v[234:241], v[34:37], v212, v213 op_sel_hi:[0,0,0]
	s_setprio 0
	s_barrier
	s_add_i32 s82, 0, 0x18000
	s_add_i32 s83, 0, 0x1c000
	v_add_u32_e32 v14, s82, v202
	v_add_u32_e32 v30, s83, v202
	ds_read_b128 v[2:5], v14
	ds_read_b128 v[6:9], v14 offset:1024
	ds_read_b128 v[10:13], v14 offset:2048
	ds_read_b128 v[14:17], v14 offset:3072
	ds_read_b128 v[18:21], v30
	ds_read_b128 v[22:25], v30 offset:1024
	ds_read_b128 v[26:29], v30 offset:2048
	ds_read_b128 v[30:33], v30 offset:3072
	s_add_u32 s48, s48, 0x40000
	s_addc_u32 s49, s49, 0
	s_mov_b32 m0, s67
	ds_read_b128 v[190:193], v211 offset:32768
	ds_read_b128 v[194:197], v211 offset:33792
	ds_read_b128 v[218:221], v211 offset:34816
	ds_read_b128 v[222:225], v211 offset:35840
	ds_read_b128 v[226:229], v211 offset:36864
	ds_read_b128 v[230:233], v211 offset:37888
	ds_read_b128 v[234:237], v211 offset:38912
	ds_read_b128 v[238:241], v211 offset:39936
	global_load_lds_dwordx4 v162, s[48:49]
	s_mov_b32 m0, s68
	s_nop 0
	global_load_lds_dwordx4 v166, s[48:49]
	s_waitcnt vmcnt(8)
	s_waitcnt lgkmcnt(0)
	s_barrier
	s_setprio 1
	s_waitcnt lgkmcnt(0)
	v_mfma_scale_f32_16x16x128_f8f6f4 v[158:161], v[2:9], v[190:197], v[158:161], v212, v213 op_sel_hi:[0,0,0]
	v_mfma_scale_f32_16x16x128_f8f6f4 v[154:157], v[10:17], v[190:197], v[154:157], v212, v213 op_sel_hi:[0,0,0]
	v_mfma_scale_f32_16x16x128_f8f6f4 v[142:145], v[2:9], v[218:225], v[142:145], v212, v213 op_sel_hi:[0,0,0]
	v_mfma_scale_f32_16x16x128_f8f6f4 v[138:141], v[10:17], v[218:225], v[138:141], v212, v213 op_sel_hi:[0,0,0]
	v_mfma_scale_f32_16x16x128_f8f6f4 v[126:129], v[2:9], v[226:233], v[126:129], v212, v213 op_sel_hi:[0,0,0]
	v_mfma_scale_f32_16x16x128_f8f6f4 v[122:125], v[10:17], v[226:233], v[122:125], v212, v213 op_sel_hi:[0,0,0]
	v_mfma_scale_f32_16x16x128_f8f6f4 v[110:113], v[2:9], v[234:241], v[110:113], v212, v213 op_sel_hi:[0,0,0]
	v_mfma_scale_f32_16x16x128_f8f6f4 v[106:109], v[10:17], v[234:241], v[106:109], v212, v213 op_sel_hi:[0,0,0]
	v_mfma_scale_f32_16x16x128_f8f6f4 v[150:153], v[18:25], v[190:197], v[150:153], v212, v213 op_sel_hi:[0,0,0]
	v_mfma_scale_f32_16x16x128_f8f6f4 v[146:149], v[26:33], v[190:197], v[146:149], v212, v213 op_sel_hi:[0,0,0]
	v_mfma_scale_f32_16x16x128_f8f6f4 v[134:137], v[18:25], v[218:225], v[134:137], v212, v213 op_sel_hi:[0,0,0]
	v_mfma_scale_f32_16x16x128_f8f6f4 v[130:133], v[26:33], v[218:225], v[130:133], v212, v213 op_sel_hi:[0,0,0]
	v_mfma_scale_f32_16x16x128_f8f6f4 v[118:121], v[18:25], v[226:233], v[118:121], v212, v213 op_sel_hi:[0,0,0]
	v_mfma_scale_f32_16x16x128_f8f6f4 v[114:117], v[26:33], v[226:233], v[114:117], v212, v213 op_sel_hi:[0,0,0]
	v_mfma_scale_f32_16x16x128_f8f6f4 v[102:105], v[18:25], v[234:241], v[102:105], v212, v213 op_sel_hi:[0,0,0]
	v_mfma_scale_f32_16x16x128_f8f6f4 v[98:101], v[26:33], v[234:241], v[98:101], v212, v213 op_sel_hi:[0,0,0]
	s_setprio 0
	s_barrier
	s_add_i32 s48, s82, s64
	v_lshl_add_u64 v[182:183], v[182:183], 0, s[24:25]
	s_mov_b32 m0, s48
	ds_read_b128 v[190:193], v211 offset:49152
	ds_read_b128 v[194:197], v211 offset:50176
	ds_read_b128 v[218:221], v211 offset:51200
	ds_read_b128 v[222:225], v211 offset:52224
	ds_read_b128 v[226:229], v211 offset:53248
	ds_read_b128 v[230:233], v211 offset:54272
	ds_read_b128 v[234:237], v211 offset:55296
	ds_read_b128 v[238:241], v211 offset:56320
	global_load_lds_dwordx4 v[182:183], off
	s_add_i32 m0, s48, 0x2000
	s_add_u32 s44, s44, 0x40080
	v_lshl_add_u64 v[182:183], v[184:185], 0, s[24:25]
	s_addc_u32 s45, s45, 0
	s_add_i32 s48, s83, s64
	global_load_lds_dwordx4 v[182:183], off
	s_mov_b32 m0, s48
	s_nop 0
	global_load_lds_dwordx4 v164, s[44:45]
	s_add_i32 m0, s48, 0x2000
	s_nop 0
	global_load_lds_dwordx4 v168, s[44:45]
	v_lshl_add_u64 v[182:183], v[186:187], 0, s[24:25]
	s_mov_b32 m0, s72
	s_nop 0
	global_load_lds_dwordx4 v[182:183], off
	v_lshl_add_u64 v[182:183], v[188:189], 0, s[24:25]
	s_mov_b32 m0, s73
	s_nop 0
	global_load_lds_dwordx4 v[182:183], off
	s_waitcnt vmcnt(8)
	s_waitcnt lgkmcnt(0)
	s_barrier
	s_setprio 1
	s_waitcnt lgkmcnt(0)
	v_mfma_scale_f32_16x16x128_f8f6f4 v[94:97], v[2:9], v[190:197], v[94:97], v212, v213 op_sel_hi:[0,0,0]
	v_mfma_scale_f32_16x16x128_f8f6f4 v[90:93], v[10:17], v[190:197], v[90:93], v212, v213 op_sel_hi:[0,0,0]
	v_mfma_scale_f32_16x16x128_f8f6f4 v[78:81], v[2:9], v[218:225], v[78:81], v212, v213 op_sel_hi:[0,0,0]
	v_mfma_scale_f32_16x16x128_f8f6f4 v[74:77], v[10:17], v[218:225], v[74:77], v212, v213 op_sel_hi:[0,0,0]
	v_mfma_scale_f32_16x16x128_f8f6f4 v[62:65], v[2:9], v[226:233], v[62:65], v212, v213 op_sel_hi:[0,0,0]
	v_mfma_scale_f32_16x16x128_f8f6f4 v[58:61], v[10:17], v[226:233], v[58:61], v212, v213 op_sel_hi:[0,0,0]
	v_mfma_scale_f32_16x16x128_f8f6f4 v[46:49], v[2:9], v[234:241], v[46:49], v212, v213 op_sel_hi:[0,0,0]
	v_mfma_scale_f32_16x16x128_f8f6f4 v[42:45], v[10:17], v[234:241], v[42:45], v212, v213 op_sel_hi:[0,0,0]
	v_mfma_scale_f32_16x16x128_f8f6f4 v[86:89], v[18:25], v[190:197], v[86:89], v212, v213 op_sel_hi:[0,0,0]
	v_mfma_scale_f32_16x16x128_f8f6f4 v[82:85], v[26:33], v[190:197], v[82:85], v212, v213 op_sel_hi:[0,0,0]
	v_mfma_scale_f32_16x16x128_f8f6f4 v[70:73], v[18:25], v[218:225], v[70:73], v212, v213 op_sel_hi:[0,0,0]
	v_mfma_scale_f32_16x16x128_f8f6f4 v[66:69], v[26:33], v[218:225], v[66:69], v212, v213 op_sel_hi:[0,0,0]
	v_mfma_scale_f32_16x16x128_f8f6f4 v[54:57], v[18:25], v[226:233], v[54:57], v212, v213 op_sel_hi:[0,0,0]
	v_mfma_scale_f32_16x16x128_f8f6f4 v[50:53], v[26:33], v[226:233], v[50:53], v212, v213 op_sel_hi:[0,0,0]
	v_mfma_scale_f32_16x16x128_f8f6f4 v[38:41], v[18:25], v[234:241], v[38:41], v212, v213 op_sel_hi:[0,0,0]
	v_mfma_scale_f32_16x16x128_f8f6f4 v[34:37], v[26:33], v[234:241], v[34:37], v212, v213 op_sel_hi:[0,0,0]
	s_setprio 0
	s_barrier
	s_add_i32 s81, s81, 2
	s_add_u32 s40, s40, 0x100
	s_addc_u32 s41, s41, 0
	s_add_u32 s60, s60, 0x100
	s_addc_u32 s61, s61, 0
	s_cmp_gt_u32 s81, 13
	s_cbranch_scc0 .LBB0_1043
	s_and_b64 vcc, exec, s[26:27]
	s_cbranch_vccz .LBB0_1046
	s_barrier

.LBB0_1257:
	ds_read_b128 v[20:23], v202
	ds_read_b128 v[166:169], v202 offset:1024
	ds_read_b128 v[14:17], v202 offset:2048
	ds_read_b128 v[162:165], v202 offset:3072
	ds_read_b128 v[8:11], v203
	ds_read_b128 v[158:161], v203 offset:1024
	ds_read_b128 v[2:5], v203 offset:2048
	ds_read_b128 v[154:157], v203 offset:3072
	s_add_u32 s22, s20, 0xfffc0080
	s_addc_u32 s23, s21, -1
	s_cmp_eq_u32 s63, 12
	s_cselect_b32 s25, s11, s23
	s_cselect_b32 s24, s49, s22
	s_cselect_b32 s23, s13, s62
	s_cselect_b32 s22, s60, s61
	s_add_i32 m0, s35, 0xc000
	ds_read_b128 v[184:187], v204
	ds_read_b128 v[188:191], v204 offset:1024
	ds_read_b128 v[206:209], v204 offset:2048
	ds_read_b128 v[222:225], v204 offset:3072
	ds_read_b128 v[212:215], v204 offset:4096
	ds_read_b128 v[226:229], v204 offset:5120
	ds_read_b128 v[218:221], v204 offset:6144
	ds_read_b128 v[230:233], v204 offset:7168
	global_load_lds_dwordx4 v180, s[20:21]
	s_add_i32 m0, s35, 0xe000
	s_nop 0
	global_load_lds_dwordx4 v182, s[20:21]
	s_waitcnt vmcnt(8)
	s_waitcnt lgkmcnt(0)
	s_barrier
	s_setprio 1
	s_waitcnt lgkmcnt(0)
	v_mov_b32_e32 v24, v166
	v_mov_b32_e32 v25, v167
	s_nop 1
	v_mfma_scale_f32_16x16x128_f8f6f4 v[150:153], v[20:25], v[184:189], v[150:153], v168, v190 op_sel_hi:[0,0,0] cbsz:2 blgp:2
	v_mov_b32_e32 v18, v162
	v_mov_b32_e32 v19, v163
	s_nop 1
	v_mfma_scale_f32_16x16x128_f8f6f4 v[138:141], v[14:19], v[184:189], v[138:141], v164, v190 op_sel_hi:[0,0,0] cbsz:2 blgp:2
	v_mov_b32_e32 v210, v222
	v_mov_b32_e32 v211, v223
	s_nop 1
	v_mfma_scale_f32_16x16x128_f8f6f4 v[134:137], v[20:25], v[206:211], v[134:137], v168, v224 op_sel_hi:[0,0,0] cbsz:2 blgp:2
	v_mfma_scale_f32_16x16x128_f8f6f4 v[122:125], v[14:19], v[206:211], v[122:125], v164, v224 op_sel_hi:[0,0,0] cbsz:2 blgp:2
	v_mov_b32_e32 v216, v226
	v_mov_b32_e32 v217, v227
	s_nop 1
	v_mfma_scale_f32_16x16x128_f8f6f4 v[118:121], v[20:25], v[212:217], v[118:121], v168, v228 op_sel_hi:[0,0,0] cbsz:2 blgp:2
	v_mfma_scale_f32_16x16x128_f8f6f4 v[106:109], v[14:19], v[212:217], v[106:109], v164, v228 op_sel_hi:[0,0,0] cbsz:2 blgp:2
	v_mov_b32_e32 v222, v230
	v_mov_b32_e32 v223, v231
	s_nop 1
	v_mfma_scale_f32_16x16x128_f8f6f4 v[102:105], v[20:25], v[218:223], v[102:105], v168, v232 op_sel_hi:[0,0,0] cbsz:2 blgp:2
	v_mfma_scale_f32_16x16x128_f8f6f4 v[90:93], v[14:19], v[218:223], v[90:93], v164, v232 op_sel_hi:[0,0,0] cbsz:2 blgp:2
	v_mov_b32_e32 v12, v158
	v_mov_b32_e32 v13, v159
	s_nop 1
	v_mfma_scale_f32_16x16x128_f8f6f4 v[146:149], v[8:13], v[184:189], v[146:149], v160, v190 op_sel_hi:[0,0,0] cbsz:2 blgp:2
	v_mov_b32_e32 v6, v154
	v_mov_b32_e32 v7, v155
	s_nop 1
	v_mfma_scale_f32_16x16x128_f8f6f4 v[142:145], v[2:7], v[184:189], v[142:145], v156, v190 op_sel_hi:[0,0,0] cbsz:2 blgp:2
	v_mfma_scale_f32_16x16x128_f8f6f4 v[130:133], v[8:13], v[206:211], v[130:133], v160, v224 op_sel_hi:[0,0,0] cbsz:2 blgp:2
	v_mfma_scale_f32_16x16x128_f8f6f4 v[126:129], v[2:7], v[206:211], v[126:129], v156, v224 op_sel_hi:[0,0,0] cbsz:2 blgp:2
	v_mfma_scale_f32_16x16x128_f8f6f4 v[114:117], v[8:13], v[212:217], v[114:117], v160, v228 op_sel_hi:[0,0,0] cbsz:2 blgp:2
	v_mfma_scale_f32_16x16x128_f8f6f4 v[110:113], v[2:7], v[212:217], v[110:113], v156, v228 op_sel_hi:[0,0,0] cbsz:2 blgp:2
	v_mfma_scale_f32_16x16x128_f8f6f4 v[98:101], v[8:13], v[218:223], v[98:101], v160, v232 op_sel_hi:[0,0,0] cbsz:2 blgp:2
	v_mfma_scale_f32_16x16x128_f8f6f4 v[94:97], v[2:7], v[218:223], v[94:97], v156, v232 op_sel_hi:[0,0,0] cbsz:2 blgp:2
	s_setprio 0
	s_barrier
	s_add_i32 s64, s42, s27
	v_lshl_add_u64 v[184:185], s[22:23], 0, v[172:173]
	s_mov_b32 m0, s64
	ds_read_b128 v[206:209], v204 offset:16384
	ds_read_b128 v[228:231], v204 offset:17408
	ds_read_b128 v[212:215], v204 offset:18432
	ds_read_b128 v[232:235], v204 offset:19456
	ds_read_b128 v[218:221], v204 offset:20480
	ds_read_b128 v[236:239], v204 offset:21504
	ds_read_b128 v[224:227], v204 offset:22528
	ds_read_b128 v[240:243], v204 offset:23552
	global_load_lds_dwordx4 v172, s[22:23]
	s_add_i32 m0, s64, 0x2000
	s_add_u32 s64, s22, 0x40000
	v_lshl_add_u64 v[186:187], s[22:23], 0, v[174:175]
	s_addc_u32 s65, s23, 0
	s_add_i32 s66, s43, s27
	global_load_lds_dwordx4 v174, s[22:23]
	s_mov_b32 m0, s66
	v_lshl_add_u64 v[188:189], s[24:25], 0, v[178:179]
	global_load_lds_dwordx4 v172, s[64:65]
	s_add_i32 m0, s66, 0x2000
	v_lshl_add_u64 v[190:191], s[24:25], 0, v[176:177]
	global_load_lds_dwordx4 v174, s[64:65]
	s_mov_b32 m0, s35
	s_nop 0
	global_load_lds_dwordx4 v178, s[24:25]
	s_mov_b32 m0, s36
	s_nop 0
	global_load_lds_dwordx4 v176, s[24:25]
	s_waitcnt vmcnt(8)
	s_waitcnt lgkmcnt(0)
	s_barrier
	s_setprio 1
	s_waitcnt lgkmcnt(0)
	v_mov_b32_e32 v210, v228
	v_mov_b32_e32 v211, v229
	s_nop 1
	v_mfma_scale_f32_16x16x128_f8f6f4 v[86:89], v[20:25], v[206:211], v[86:89], v168, v230 op_sel_hi:[0,0,0] cbsz:2 blgp:2
	v_mfma_scale_f32_16x16x128_f8f6f4 v[74:77], v[14:19], v[206:211], v[74:77], v164, v230 op_sel_hi:[0,0,0] cbsz:2 blgp:2
	v_mov_b32_e32 v216, v232
	v_mov_b32_e32 v217, v233
	s_nop 1
	v_mfma_scale_f32_16x16x128_f8f6f4 v[70:73], v[20:25], v[212:217], v[70:73], v168, v234 op_sel_hi:[0,0,0] cbsz:2 blgp:2
	v_mfma_scale_f32_16x16x128_f8f6f4 v[58:61], v[14:19], v[212:217], v[58:61], v164, v234 op_sel_hi:[0,0,0] cbsz:2 blgp:2
	v_mov_b32_e32 v222, v236
	v_mov_b32_e32 v223, v237
	s_nop 1
	v_mfma_scale_f32_16x16x128_f8f6f4 v[54:57], v[20:25], v[218:223], v[54:57], v168, v238 op_sel_hi:[0,0,0] cbsz:2 blgp:2
	v_mfma_scale_f32_16x16x128_f8f6f4 v[42:45], v[14:19], v[218:223], v[42:45], v164, v238 op_sel_hi:[0,0,0] cbsz:2 blgp:2
	v_mov_b32_e32 v228, v240
	v_mov_b32_e32 v229, v241
	s_nop 1
	v_mfma_scale_f32_16x16x128_f8f6f4 v[38:41], v[20:25], v[224:229], v[38:41], v168, v242 op_sel_hi:[0,0,0] cbsz:2 blgp:2
	v_mfma_scale_f32_16x16x128_f8f6f4 v[26:29], v[14:19], v[224:229], v[26:29], v164, v242 op_sel_hi:[0,0,0] cbsz:2 blgp:2
	v_mfma_scale_f32_16x16x128_f8f6f4 v[82:85], v[8:13], v[206:211], v[82:85], v160, v230 op_sel_hi:[0,0,0] cbsz:2 blgp:2
	v_mfma_scale_f32_16x16x128_f8f6f4 v[78:81], v[2:7], v[206:211], v[78:81], v156, v230 op_sel_hi:[0,0,0] cbsz:2 blgp:2
	v_mfma_scale_f32_16x16x128_f8f6f4 v[66:69], v[8:13], v[212:217], v[66:69], v160, v234 op_sel_hi:[0,0,0] cbsz:2 blgp:2
	v_mfma_scale_f32_16x16x128_f8f6f4 v[62:65], v[2:7], v[212:217], v[62:65], v156, v234 op_sel_hi:[0,0,0] cbsz:2 blgp:2
	v_mfma_scale_f32_16x16x128_f8f6f4 v[50:53], v[8:13], v[218:223], v[50:53], v160, v238 op_sel_hi:[0,0,0] cbsz:2 blgp:2
	v_mfma_scale_f32_16x16x128_f8f6f4 v[46:49], v[2:7], v[218:223], v[46:49], v156, v238 op_sel_hi:[0,0,0] cbsz:2 blgp:2
	v_mfma_scale_f32_16x16x128_f8f6f4 v[34:37], v[8:13], v[224:229], v[34:37], v160, v242 op_sel_hi:[0,0,0] cbsz:2 blgp:2
	v_mfma_scale_f32_16x16x128_f8f6f4 v[30:33], v[2:7], v[224:229], v[30:33], v156, v242 op_sel_hi:[0,0,0] cbsz:2 blgp:2
	s_setprio 0
	s_barrier
	s_add_i32 s64, 0, 0x18000
	s_add_i32 s65, 0, 0x1c000
	v_add_u32_e32 v2, s64, v198
	v_add_u32_e32 v6, s65, v198
	ds_read_b128 v[20:23], v2
	ds_read_b128 v[166:169], v2 offset:1024
	ds_read_b128 v[14:17], v2 offset:2048
	ds_read_b128 v[162:165], v2 offset:3072
	ds_read_b128 v[8:11], v6
	ds_read_b128 v[154:157], v6 offset:1024
	ds_read_b128 v[2:5], v6 offset:2048
	ds_read_b128 v[158:161], v6 offset:3072
	s_add_u32 s24, s24, 0x40000
	s_addc_u32 s25, s25, 0
	s_mov_b32 m0, s37
	ds_read_b128 v[206:209], v204 offset:32768
	ds_read_b128 v[228:231], v204 offset:33792
	ds_read_b128 v[212:215], v204 offset:34816
	ds_read_b128 v[232:235], v204 offset:35840
	ds_read_b128 v[218:221], v204 offset:36864
	ds_read_b128 v[236:239], v204 offset:37888
	ds_read_b128 v[224:227], v204 offset:38912
	ds_read_b128 v[240:243], v204 offset:39936
	global_load_lds_dwordx4 v178, s[24:25]
	s_mov_b32 m0, s38
	s_nop 0
	global_load_lds_dwordx4 v176, s[24:25]
	s_waitcnt vmcnt(8)
	s_waitcnt lgkmcnt(0)
	s_barrier
	s_setprio 1
	s_waitcnt lgkmcnt(0)
	v_mov_b32_e32 v24, v166
	v_mov_b32_e32 v25, v167
	v_mov_b32_e32 v210, v228
	v_mov_b32_e32 v211, v229
	s_nop 1
	v_mfma_scale_f32_16x16x128_f8f6f4 v[150:153], v[20:25], v[206:211], v[150:153], v168, v230 op_sel_hi:[0,0,0] cbsz:2 blgp:2
	v_mov_b32_e32 v18, v162
	v_mov_b32_e32 v19, v163
	s_nop 1
	v_mfma_scale_f32_16x16x128_f8f6f4 v[138:141], v[14:19], v[206:211], v[138:141], v164, v230 op_sel_hi:[0,0,0] cbsz:2 blgp:2
	v_mov_b32_e32 v216, v232
	v_mov_b32_e32 v217, v233
	s_nop 1
	v_mfma_scale_f32_16x16x128_f8f6f4 v[134:137], v[20:25], v[212:217], v[134:137], v168, v234 op_sel_hi:[0,0,0] cbsz:2 blgp:2
	v_mfma_scale_f32_16x16x128_f8f6f4 v[122:125], v[14:19], v[212:217], v[122:125], v164, v234 op_sel_hi:[0,0,0] cbsz:2 blgp:2
	v_mov_b32_e32 v222, v236
	v_mov_b32_e32 v223, v237
	s_nop 1
	v_mfma_scale_f32_16x16x128_f8f6f4 v[118:121], v[20:25], v[218:223], v[118:121], v168, v238 op_sel_hi:[0,0,0] cbsz:2 blgp:2
	v_mfma_scale_f32_16x16x128_f8f6f4 v[106:109], v[14:19], v[218:223], v[106:109], v164, v238 op_sel_hi:[0,0,0] cbsz:2 blgp:2
	v_mov_b32_e32 v228, v240
	v_mov_b32_e32 v229, v241
	s_nop 1
	v_mfma_scale_f32_16x16x128_f8f6f4 v[102:105], v[20:25], v[224:229], v[102:105], v168, v242 op_sel_hi:[0,0,0] cbsz:2 blgp:2
	v_mfma_scale_f32_16x16x128_f8f6f4 v[90:93], v[14:19], v[224:229], v[90:93], v164, v242 op_sel_hi:[0,0,0] cbsz:2 blgp:2
	v_mov_b32_e32 v12, v154
	v_mov_b32_e32 v13, v155
	s_nop 1
	v_mfma_scale_f32_16x16x128_f8f6f4 v[146:149], v[8:13], v[206:211], v[146:149], v156, v230 op_sel_hi:[0,0,0] cbsz:2 blgp:2
	v_mov_b32_e32 v6, v158
	v_mov_b32_e32 v7, v159
	s_nop 1
	v_mfma_scale_f32_16x16x128_f8f6f4 v[142:145], v[2:7], v[206:211], v[142:145], v160, v230 op_sel_hi:[0,0,0] cbsz:2 blgp:2
	v_mfma_scale_f32_16x16x128_f8f6f4 v[130:133], v[8:13], v[212:217], v[130:133], v156, v234 op_sel_hi:[0,0,0] cbsz:2 blgp:2
	v_mfma_scale_f32_16x16x128_f8f6f4 v[126:129], v[2:7], v[212:217], v[126:129], v160, v234 op_sel_hi:[0,0,0] cbsz:2 blgp:2
	v_mfma_scale_f32_16x16x128_f8f6f4 v[114:117], v[8:13], v[218:223], v[114:117], v156, v238 op_sel_hi:[0,0,0] cbsz:2 blgp:2
	v_mfma_scale_f32_16x16x128_f8f6f4 v[110:113], v[2:7], v[218:223], v[110:113], v160, v238 op_sel_hi:[0,0,0] cbsz:2 blgp:2
	v_mfma_scale_f32_16x16x128_f8f6f4 v[98:101], v[8:13], v[224:229], v[98:101], v156, v242 op_sel_hi:[0,0,0] cbsz:2 blgp:2
	v_mfma_scale_f32_16x16x128_f8f6f4 v[94:97], v[2:7], v[224:229], v[94:97], v160, v242 op_sel_hi:[0,0,0] cbsz:2 blgp:2
	s_setprio 0
	s_barrier
	s_add_i32 s24, s64, s27
	v_lshl_add_u64 v[154:155], v[184:185], 0, s[6:7]
	s_mov_b32 m0, s24
	ds_read_b128 v[206:209], v204 offset:49152
	ds_read_b128 v[228:231], v204 offset:50176
	ds_read_b128 v[212:215], v204 offset:51200
	ds_read_b128 v[232:235], v204 offset:52224
	ds_read_b128 v[218:221], v204 offset:53248
	ds_read_b128 v[236:239], v204 offset:54272
	ds_read_b128 v[224:227], v204 offset:55296
	ds_read_b128 v[240:243], v204 offset:56320
	global_load_lds_dwordx4 v[154:155], off
	s_add_i32 m0, s24, 0x2000
	s_add_u32 s22, s22, 0x40080
	v_lshl_add_u64 v[154:155], v[186:187], 0, s[6:7]
	s_addc_u32 s23, s23, 0
	s_add_i32 s24, s65, s27
	global_load_lds_dwordx4 v[154:155], off
	s_mov_b32 m0, s24
	s_nop 0
	global_load_lds_dwordx4 v172, s[22:23]
	s_add_i32 m0, s24, 0x2000
	s_nop 0
	global_load_lds_dwordx4 v174, s[22:23]
	v_lshl_add_u64 v[154:155], v[188:189], 0, s[6:7]
	s_mov_b32 m0, s39
	s_nop 0
	global_load_lds_dwordx4 v[154:155], off
	v_lshl_add_u64 v[154:155], v[190:191], 0, s[6:7]
	s_mov_b32 m0, s40
	s_nop 0
	global_load_lds_dwordx4 v[154:155], off
	s_waitcnt vmcnt(8)
	s_waitcnt lgkmcnt(0)
	s_barrier
	s_setprio 1
	s_waitcnt lgkmcnt(0)
	v_mov_b32_e32 v210, v228
	v_mov_b32_e32 v211, v229
	s_nop 1
	v_mfma_scale_f32_16x16x128_f8f6f4 v[86:89], v[20:25], v[206:211], v[86:89], v168, v230 op_sel_hi:[0,0,0] cbsz:2 blgp:2
	v_mfma_scale_f32_16x16x128_f8f6f4 v[74:77], v[14:19], v[206:211], v[74:77], v164, v230 op_sel_hi:[0,0,0] cbsz:2 blgp:2
	v_mov_b32_e32 v216, v232
	v_mov_b32_e32 v217, v233
	s_nop 1
	v_mfma_scale_f32_16x16x128_f8f6f4 v[70:73], v[20:25], v[212:217], v[70:73], v168, v234 op_sel_hi:[0,0,0] cbsz:2 blgp:2
	v_mfma_scale_f32_16x16x128_f8f6f4 v[58:61], v[14:19], v[212:217], v[58:61], v164, v234 op_sel_hi:[0,0,0] cbsz:2 blgp:2
	v_mov_b32_e32 v222, v236
	v_mov_b32_e32 v223, v237
	s_nop 1
	v_mfma_scale_f32_16x16x128_f8f6f4 v[54:57], v[20:25], v[218:223], v[54:57], v168, v238 op_sel_hi:[0,0,0] cbsz:2 blgp:2
	v_mfma_scale_f32_16x16x128_f8f6f4 v[42:45], v[14:19], v[218:223], v[42:45], v164, v238 op_sel_hi:[0,0,0] cbsz:2 blgp:2
	v_mov_b32_e32 v228, v240
	v_mov_b32_e32 v229, v241
	s_nop 1
	v_mfma_scale_f32_16x16x128_f8f6f4 v[38:41], v[20:25], v[224:229], v[38:41], v168, v242 op_sel_hi:[0,0,0] cbsz:2 blgp:2
	v_mfma_scale_f32_16x16x128_f8f6f4 v[26:29], v[14:19], v[224:229], v[26:29], v164, v242 op_sel_hi:[0,0,0] cbsz:2 blgp:2
	v_mfma_scale_f32_16x16x128_f8f6f4 v[82:85], v[8:13], v[206:211], v[82:85], v156, v230 op_sel_hi:[0,0,0] cbsz:2 blgp:2
	v_mfma_scale_f32_16x16x128_f8f6f4 v[78:81], v[2:7], v[206:211], v[78:81], v160, v230 op_sel_hi:[0,0,0] cbsz:2 blgp:2
	v_mfma_scale_f32_16x16x128_f8f6f4 v[66:69], v[8:13], v[212:217], v[66:69], v156, v234 op_sel_hi:[0,0,0] cbsz:2 blgp:2
	v_mfma_scale_f32_16x16x128_f8f6f4 v[62:65], v[2:7], v[212:217], v[62:65], v160, v234 op_sel_hi:[0,0,0] cbsz:2 blgp:2
	v_mfma_scale_f32_16x16x128_f8f6f4 v[50:53], v[8:13], v[218:223], v[50:53], v156, v238 op_sel_hi:[0,0,0] cbsz:2 blgp:2
	v_mfma_scale_f32_16x16x128_f8f6f4 v[46:49], v[2:7], v[218:223], v[46:49], v160, v238 op_sel_hi:[0,0,0] cbsz:2 blgp:2
	v_mfma_scale_f32_16x16x128_f8f6f4 v[34:37], v[8:13], v[224:229], v[34:37], v156, v242 op_sel_hi:[0,0,0] cbsz:2 blgp:2
	v_mfma_scale_f32_16x16x128_f8f6f4 v[30:33], v[2:7], v[224:229], v[30:33], v160, v242 op_sel_hi:[0,0,0] cbsz:2 blgp:2
	s_setprio 0
	s_barrier
	s_add_i32 s63, s63, 2
	s_add_u32 s20, s20, 0x100
	s_addc_u32 s21, s21, 0
	s_add_u32 s61, s61, 0x100
	s_addc_u32 s62, s62, 0
	s_cmp_gt_u32 s63, 13
	s_cbranch_scc0 .LBB0_1257
	s_and_b64 vcc, exec, s[8:9]
	s_cbranch_vccz .LBB0_1260
	s_barrier

.LBB0_1279:
	ds_read_b128 v[20:23], v195
	ds_read_b128 v[166:169], v195 offset:1024
	ds_read_b128 v[14:17], v195 offset:2048
	ds_read_b128 v[162:165], v195 offset:3072
	ds_read_b128 v[8:11], v196
	ds_read_b128 v[158:161], v196 offset:1024
	ds_read_b128 v[2:5], v196 offset:2048
	ds_read_b128 v[154:157], v196 offset:3072
	s_add_u32 s24, s22, 0xfffc0080
	s_addc_u32 s25, s23, -1
	s_cmp_eq_u32 s61, 12
	s_cselect_b32 s27, s11, s25
	s_cselect_b32 s26, s49, s24
	s_cselect_b32 s25, s13, s60
	s_cselect_b32 s24, s50, s51
	s_mov_b32 m0, s46
	ds_read_b128 v[184:187], v198
	ds_read_b128 v[188:191], v198 offset:1024
	ds_read_b128 v[202:205], v198 offset:2048
	ds_read_b128 v[218:221], v198 offset:3072
	ds_read_b128 v[208:211], v198 offset:4096
	ds_read_b128 v[222:225], v198 offset:5120
	ds_read_b128 v[214:217], v198 offset:6144
	ds_read_b128 v[226:229], v198 offset:7168
	global_load_lds_dwordx4 v180, s[22:23]
	s_add_i32 m0, s21, 0xe000
	s_nop 0
	global_load_lds_dwordx4 v182, s[22:23]
	s_waitcnt vmcnt(8)
	s_waitcnt lgkmcnt(0)
	s_barrier
	s_setprio 1
	s_waitcnt lgkmcnt(0)
	v_mov_b32_e32 v24, v166
	v_mov_b32_e32 v25, v167
	s_nop 1
	v_mfma_scale_f32_16x16x128_f8f6f4 v[150:153], v[20:25], v[184:189], v[150:153], v168, v190 op_sel_hi:[0,0,0] cbsz:2 blgp:2
	v_mov_b32_e32 v18, v162
	v_mov_b32_e32 v19, v163
	s_nop 1
	v_mfma_scale_f32_16x16x128_f8f6f4 v[138:141], v[14:19], v[184:189], v[138:141], v164, v190 op_sel_hi:[0,0,0] cbsz:2 blgp:2
	v_mov_b32_e32 v206, v218
	v_mov_b32_e32 v207, v219
	s_nop 1
	v_mfma_scale_f32_16x16x128_f8f6f4 v[134:137], v[20:25], v[202:207], v[134:137], v168, v220 op_sel_hi:[0,0,0] cbsz:2 blgp:2
	v_mfma_scale_f32_16x16x128_f8f6f4 v[122:125], v[14:19], v[202:207], v[122:125], v164, v220 op_sel_hi:[0,0,0] cbsz:2 blgp:2
	v_mov_b32_e32 v212, v222
	v_mov_b32_e32 v213, v223
	s_nop 1
	v_mfma_scale_f32_16x16x128_f8f6f4 v[118:121], v[20:25], v[208:213], v[118:121], v168, v224 op_sel_hi:[0,0,0] cbsz:2 blgp:2
	v_mfma_scale_f32_16x16x128_f8f6f4 v[106:109], v[14:19], v[208:213], v[106:109], v164, v224 op_sel_hi:[0,0,0] cbsz:2 blgp:2
	v_mov_b32_e32 v218, v226
	v_mov_b32_e32 v219, v227
	s_nop 1
	v_mfma_scale_f32_16x16x128_f8f6f4 v[102:105], v[20:25], v[214:219], v[102:105], v168, v228 op_sel_hi:[0,0,0] cbsz:2 blgp:2
	v_mfma_scale_f32_16x16x128_f8f6f4 v[90:93], v[14:19], v[214:219], v[90:93], v164, v228 op_sel_hi:[0,0,0] cbsz:2 blgp:2
	v_mov_b32_e32 v12, v158
	v_mov_b32_e32 v13, v159
	s_nop 1
	v_mfma_scale_f32_16x16x128_f8f6f4 v[146:149], v[8:13], v[184:189], v[146:149], v160, v190 op_sel_hi:[0,0,0] cbsz:2 blgp:2
	v_mov_b32_e32 v6, v154
	v_mov_b32_e32 v7, v155
	s_nop 1
	v_mfma_scale_f32_16x16x128_f8f6f4 v[142:145], v[2:7], v[184:189], v[142:145], v156, v190 op_sel_hi:[0,0,0] cbsz:2 blgp:2
	v_mfma_scale_f32_16x16x128_f8f6f4 v[130:133], v[8:13], v[202:207], v[130:133], v160, v220 op_sel_hi:[0,0,0] cbsz:2 blgp:2
	v_mfma_scale_f32_16x16x128_f8f6f4 v[126:129], v[2:7], v[202:207], v[126:129], v156, v220 op_sel_hi:[0,0,0] cbsz:2 blgp:2
	v_mfma_scale_f32_16x16x128_f8f6f4 v[114:117], v[8:13], v[208:213], v[114:117], v160, v224 op_sel_hi:[0,0,0] cbsz:2 blgp:2
	v_mfma_scale_f32_16x16x128_f8f6f4 v[110:113], v[2:7], v[208:213], v[110:113], v156, v224 op_sel_hi:[0,0,0] cbsz:2 blgp:2
	v_mfma_scale_f32_16x16x128_f8f6f4 v[98:101], v[8:13], v[214:219], v[98:101], v160, v228 op_sel_hi:[0,0,0] cbsz:2 blgp:2
	v_mfma_scale_f32_16x16x128_f8f6f4 v[94:97], v[2:7], v[214:219], v[94:97], v156, v228 op_sel_hi:[0,0,0] cbsz:2 blgp:2
	s_setprio 0
	s_barrier
	s_add_i32 s62, s42, s35
	v_lshl_add_u64 v[184:185], s[24:25], 0, v[176:177]
	s_mov_b32 m0, s62
	ds_read_b128 v[202:205], v198 offset:16384
	ds_read_b128 v[224:227], v198 offset:17408
	ds_read_b128 v[208:211], v198 offset:18432
	ds_read_b128 v[228:231], v198 offset:19456
	ds_read_b128 v[214:217], v198 offset:20480
	ds_read_b128 v[232:235], v198 offset:21504
	ds_read_b128 v[220:223], v198 offset:22528
	ds_read_b128 v[236:239], v198 offset:23552
	global_load_lds_dwordx4 v176, s[24:25]
	s_add_i32 m0, s62, 0x2000
	s_add_u32 s62, s24, 0x40000
	v_lshl_add_u64 v[186:187], s[24:25], 0, v[172:173]
	s_addc_u32 s63, s25, 0
	s_add_i32 s64, s43, s35
	global_load_lds_dwordx4 v172, s[24:25]
	s_mov_b32 m0, s64
	v_lshl_add_u64 v[188:189], s[26:27], 0, v[178:179]
	global_load_lds_dwordx4 v176, s[62:63]
	s_add_i32 m0, s64, 0x2000
	v_lshl_add_u64 v[190:191], s[26:27], 0, v[174:175]
	global_load_lds_dwordx4 v172, s[62:63]
	s_mov_b32 m0, s21
	s_nop 0
	global_load_lds_dwordx4 v178, s[26:27]
	s_mov_b32 m0, s36
	s_nop 0
	global_load_lds_dwordx4 v174, s[26:27]
	s_waitcnt vmcnt(8)
	s_waitcnt lgkmcnt(0)
	s_barrier
	s_setprio 1
	s_waitcnt lgkmcnt(0)
	v_mov_b32_e32 v206, v224
	v_mov_b32_e32 v207, v225
	s_nop 1
	v_mfma_scale_f32_16x16x128_f8f6f4 v[86:89], v[20:25], v[202:207], v[86:89], v168, v226 op_sel_hi:[0,0,0] cbsz:2 blgp:2
	v_mfma_scale_f32_16x16x128_f8f6f4 v[74:77], v[14:19], v[202:207], v[74:77], v164, v226 op_sel_hi:[0,0,0] cbsz:2 blgp:2
	v_mov_b32_e32 v212, v228
	v_mov_b32_e32 v213, v229
	s_nop 1
	v_mfma_scale_f32_16x16x128_f8f6f4 v[70:73], v[20:25], v[208:213], v[70:73], v168, v230 op_sel_hi:[0,0,0] cbsz:2 blgp:2
	v_mfma_scale_f32_16x16x128_f8f6f4 v[58:61], v[14:19], v[208:213], v[58:61], v164, v230 op_sel_hi:[0,0,0] cbsz:2 blgp:2
	v_mov_b32_e32 v218, v232
	v_mov_b32_e32 v219, v233
	s_nop 1
	v_mfma_scale_f32_16x16x128_f8f6f4 v[54:57], v[20:25], v[214:219], v[54:57], v168, v234 op_sel_hi:[0,0,0] cbsz:2 blgp:2
	v_mfma_scale_f32_16x16x128_f8f6f4 v[42:45], v[14:19], v[214:219], v[42:45], v164, v234 op_sel_hi:[0,0,0] cbsz:2 blgp:2
	v_mov_b32_e32 v224, v236
	v_mov_b32_e32 v225, v237
	s_nop 1
	v_mfma_scale_f32_16x16x128_f8f6f4 v[38:41], v[20:25], v[220:225], v[38:41], v168, v238 op_sel_hi:[0,0,0] cbsz:2 blgp:2
	v_mfma_scale_f32_16x16x128_f8f6f4 v[26:29], v[14:19], v[220:225], v[26:29], v164, v238 op_sel_hi:[0,0,0] cbsz:2 blgp:2
	v_mfma_scale_f32_16x16x128_f8f6f4 v[82:85], v[8:13], v[202:207], v[82:85], v160, v226 op_sel_hi:[0,0,0] cbsz:2 blgp:2
	v_mfma_scale_f32_16x16x128_f8f6f4 v[78:81], v[2:7], v[202:207], v[78:81], v156, v226 op_sel_hi:[0,0,0] cbsz:2 blgp:2
	v_mfma_scale_f32_16x16x128_f8f6f4 v[66:69], v[8:13], v[208:213], v[66:69], v160, v230 op_sel_hi:[0,0,0] cbsz:2 blgp:2
	v_mfma_scale_f32_16x16x128_f8f6f4 v[62:65], v[2:7], v[208:213], v[62:65], v156, v230 op_sel_hi:[0,0,0] cbsz:2 blgp:2
	v_mfma_scale_f32_16x16x128_f8f6f4 v[50:53], v[8:13], v[214:219], v[50:53], v160, v234 op_sel_hi:[0,0,0] cbsz:2 blgp:2
	v_mfma_scale_f32_16x16x128_f8f6f4 v[46:49], v[2:7], v[214:219], v[46:49], v156, v234 op_sel_hi:[0,0,0] cbsz:2 blgp:2
	v_mfma_scale_f32_16x16x128_f8f6f4 v[34:37], v[8:13], v[220:225], v[34:37], v160, v238 op_sel_hi:[0,0,0] cbsz:2 blgp:2
	v_mfma_scale_f32_16x16x128_f8f6f4 v[30:33], v[2:7], v[220:225], v[30:33], v156, v238 op_sel_hi:[0,0,0] cbsz:2 blgp:2
	s_setprio 0
	s_barrier
	s_add_i32 s62, 0, 0x18000
	s_add_i32 s63, 0, 0x1c000
	v_add_u32_e32 v2, s62, v194
	v_add_u32_e32 v6, s63, v194
	ds_read_b128 v[20:23], v2
	ds_read_b128 v[166:169], v2 offset:1024
	ds_read_b128 v[14:17], v2 offset:2048
	ds_read_b128 v[162:165], v2 offset:3072
	ds_read_b128 v[8:11], v6
	ds_read_b128 v[154:157], v6 offset:1024
	ds_read_b128 v[2:5], v6 offset:2048
	ds_read_b128 v[158:161], v6 offset:3072
	s_add_u32 s26, s26, 0x40000
	s_addc_u32 s27, s27, 0
	s_mov_b32 m0, s37
	ds_read_b128 v[202:205], v198 offset:32768
	ds_read_b128 v[224:227], v198 offset:33792
	ds_read_b128 v[208:211], v198 offset:34816
	ds_read_b128 v[228:231], v198 offset:35840
	ds_read_b128 v[214:217], v198 offset:36864
	ds_read_b128 v[232:235], v198 offset:37888
	ds_read_b128 v[220:223], v198 offset:38912
	ds_read_b128 v[236:239], v198 offset:39936
	global_load_lds_dwordx4 v178, s[26:27]
	s_mov_b32 m0, s38
	s_nop 0
	global_load_lds_dwordx4 v174, s[26:27]
	s_waitcnt vmcnt(8)
	s_waitcnt lgkmcnt(0)
	s_barrier
	s_setprio 1
	s_waitcnt lgkmcnt(0)
	v_mov_b32_e32 v24, v166
	v_mov_b32_e32 v25, v167
	v_mov_b32_e32 v206, v224
	v_mov_b32_e32 v207, v225
	s_nop 1
	v_mfma_scale_f32_16x16x128_f8f6f4 v[150:153], v[20:25], v[202:207], v[150:153], v168, v226 op_sel_hi:[0,0,0] cbsz:2 blgp:2
	v_mov_b32_e32 v18, v162
	v_mov_b32_e32 v19, v163
	s_nop 1
	v_mfma_scale_f32_16x16x128_f8f6f4 v[138:141], v[14:19], v[202:207], v[138:141], v164, v226 op_sel_hi:[0,0,0] cbsz:2 blgp:2
	v_mov_b32_e32 v212, v228
	v_mov_b32_e32 v213, v229
	s_nop 1
	v_mfma_scale_f32_16x16x128_f8f6f4 v[134:137], v[20:25], v[208:213], v[134:137], v168, v230 op_sel_hi:[0,0,0] cbsz:2 blgp:2
	v_mfma_scale_f32_16x16x128_f8f6f4 v[122:125], v[14:19], v[208:213], v[122:125], v164, v230 op_sel_hi:[0,0,0] cbsz:2 blgp:2
	v_mov_b32_e32 v218, v232
	v_mov_b32_e32 v219, v233
	s_nop 1
	v_mfma_scale_f32_16x16x128_f8f6f4 v[118:121], v[20:25], v[214:219], v[118:121], v168, v234 op_sel_hi:[0,0,0] cbsz:2 blgp:2
	v_mfma_scale_f32_16x16x128_f8f6f4 v[106:109], v[14:19], v[214:219], v[106:109], v164, v234 op_sel_hi:[0,0,0] cbsz:2 blgp:2
	v_mov_b32_e32 v224, v236
	v_mov_b32_e32 v225, v237
	s_nop 1
	v_mfma_scale_f32_16x16x128_f8f6f4 v[102:105], v[20:25], v[220:225], v[102:105], v168, v238 op_sel_hi:[0,0,0] cbsz:2 blgp:2
	v_mfma_scale_f32_16x16x128_f8f6f4 v[90:93], v[14:19], v[220:225], v[90:93], v164, v238 op_sel_hi:[0,0,0] cbsz:2 blgp:2
	v_mov_b32_e32 v12, v154
	v_mov_b32_e32 v13, v155
	s_nop 1
	v_mfma_scale_f32_16x16x128_f8f6f4 v[146:149], v[8:13], v[202:207], v[146:149], v156, v226 op_sel_hi:[0,0,0] cbsz:2 blgp:2
	v_mov_b32_e32 v6, v158
	v_mov_b32_e32 v7, v159
	s_nop 1
	v_mfma_scale_f32_16x16x128_f8f6f4 v[142:145], v[2:7], v[202:207], v[142:145], v160, v226 op_sel_hi:[0,0,0] cbsz:2 blgp:2
	v_mfma_scale_f32_16x16x128_f8f6f4 v[130:133], v[8:13], v[208:213], v[130:133], v156, v230 op_sel_hi:[0,0,0] cbsz:2 blgp:2
	v_mfma_scale_f32_16x16x128_f8f6f4 v[126:129], v[2:7], v[208:213], v[126:129], v160, v230 op_sel_hi:[0,0,0] cbsz:2 blgp:2
	v_mfma_scale_f32_16x16x128_f8f6f4 v[114:117], v[8:13], v[214:219], v[114:117], v156, v234 op_sel_hi:[0,0,0] cbsz:2 blgp:2
	v_mfma_scale_f32_16x16x128_f8f6f4 v[110:113], v[2:7], v[214:219], v[110:113], v160, v234 op_sel_hi:[0,0,0] cbsz:2 blgp:2
	v_mfma_scale_f32_16x16x128_f8f6f4 v[98:101], v[8:13], v[220:225], v[98:101], v156, v238 op_sel_hi:[0,0,0] cbsz:2 blgp:2
	v_mfma_scale_f32_16x16x128_f8f6f4 v[94:97], v[2:7], v[220:225], v[94:97], v160, v238 op_sel_hi:[0,0,0] cbsz:2 blgp:2
	s_setprio 0
	s_barrier
	s_add_i32 s26, s62, s35
	v_lshl_add_u64 v[154:155], v[184:185], 0, s[6:7]
	s_mov_b32 m0, s26
	ds_read_b128 v[202:205], v198 offset:49152
	ds_read_b128 v[224:227], v198 offset:50176
	ds_read_b128 v[208:211], v198 offset:51200
	ds_read_b128 v[228:231], v198 offset:52224
	ds_read_b128 v[214:217], v198 offset:53248
	ds_read_b128 v[232:235], v198 offset:54272
	ds_read_b128 v[220:223], v198 offset:55296
	ds_read_b128 v[236:239], v198 offset:56320
	global_load_lds_dwordx4 v[154:155], off
	s_add_i32 m0, s26, 0x2000
	s_add_u32 s24, s24, 0x40080
	v_lshl_add_u64 v[154:155], v[186:187], 0, s[6:7]
	s_addc_u32 s25, s25, 0
	s_add_i32 s26, s63, s35
	global_load_lds_dwordx4 v[154:155], off
	s_mov_b32 m0, s26
	s_nop 0
	global_load_lds_dwordx4 v176, s[24:25]
	s_add_i32 m0, s26, 0x2000
	s_nop 0
	global_load_lds_dwordx4 v172, s[24:25]
	v_lshl_add_u64 v[154:155], v[188:189], 0, s[6:7]
	s_mov_b32 m0, s40
	s_nop 0
	global_load_lds_dwordx4 v[154:155], off
	v_lshl_add_u64 v[154:155], v[190:191], 0, s[6:7]
	s_mov_b32 m0, s41
	s_nop 0
	global_load_lds_dwordx4 v[154:155], off
	s_waitcnt vmcnt(8)
	s_waitcnt lgkmcnt(0)
	s_barrier
	s_setprio 1
	s_waitcnt lgkmcnt(0)
	v_mov_b32_e32 v206, v224
	v_mov_b32_e32 v207, v225
	s_nop 1
	v_mfma_scale_f32_16x16x128_f8f6f4 v[86:89], v[20:25], v[202:207], v[86:89], v168, v226 op_sel_hi:[0,0,0] cbsz:2 blgp:2
	v_mfma_scale_f32_16x16x128_f8f6f4 v[74:77], v[14:19], v[202:207], v[74:77], v164, v226 op_sel_hi:[0,0,0] cbsz:2 blgp:2
	v_mov_b32_e32 v212, v228
	v_mov_b32_e32 v213, v229
	s_nop 1
	v_mfma_scale_f32_16x16x128_f8f6f4 v[70:73], v[20:25], v[208:213], v[70:73], v168, v230 op_sel_hi:[0,0,0] cbsz:2 blgp:2
	v_mfma_scale_f32_16x16x128_f8f6f4 v[58:61], v[14:19], v[208:213], v[58:61], v164, v230 op_sel_hi:[0,0,0] cbsz:2 blgp:2
	v_mov_b32_e32 v218, v232
	v_mov_b32_e32 v219, v233
	s_nop 1
	v_mfma_scale_f32_16x16x128_f8f6f4 v[54:57], v[20:25], v[214:219], v[54:57], v168, v234 op_sel_hi:[0,0,0] cbsz:2 blgp:2
	v_mfma_scale_f32_16x16x128_f8f6f4 v[42:45], v[14:19], v[214:219], v[42:45], v164, v234 op_sel_hi:[0,0,0] cbsz:2 blgp:2
	v_mov_b32_e32 v224, v236
	v_mov_b32_e32 v225, v237
	s_nop 1
	v_mfma_scale_f32_16x16x128_f8f6f4 v[38:41], v[20:25], v[220:225], v[38:41], v168, v238 op_sel_hi:[0,0,0] cbsz:2 blgp:2
	v_mfma_scale_f32_16x16x128_f8f6f4 v[26:29], v[14:19], v[220:225], v[26:29], v164, v238 op_sel_hi:[0,0,0] cbsz:2 blgp:2
	v_mfma_scale_f32_16x16x128_f8f6f4 v[82:85], v[8:13], v[202:207], v[82:85], v156, v226 op_sel_hi:[0,0,0] cbsz:2 blgp:2
	v_mfma_scale_f32_16x16x128_f8f6f4 v[78:81], v[2:7], v[202:207], v[78:81], v160, v226 op_sel_hi:[0,0,0] cbsz:2 blgp:2
	v_mfma_scale_f32_16x16x128_f8f6f4 v[66:69], v[8:13], v[208:213], v[66:69], v156, v230 op_sel_hi:[0,0,0] cbsz:2 blgp:2
	v_mfma_scale_f32_16x16x128_f8f6f4 v[62:65], v[2:7], v[208:213], v[62:65], v160, v230 op_sel_hi:[0,0,0] cbsz:2 blgp:2
	v_mfma_scale_f32_16x16x128_f8f6f4 v[50:53], v[8:13], v[214:219], v[50:53], v156, v234 op_sel_hi:[0,0,0] cbsz:2 blgp:2
	v_mfma_scale_f32_16x16x128_f8f6f4 v[46:49], v[2:7], v[214:219], v[46:49], v160, v234 op_sel_hi:[0,0,0] cbsz:2 blgp:2
	v_mfma_scale_f32_16x16x128_f8f6f4 v[34:37], v[8:13], v[220:225], v[34:37], v156, v238 op_sel_hi:[0,0,0] cbsz:2 blgp:2
	v_mfma_scale_f32_16x16x128_f8f6f4 v[30:33], v[2:7], v[220:225], v[30:33], v160, v238 op_sel_hi:[0,0,0] cbsz:2 blgp:2
	s_setprio 0
	s_barrier
	s_add_i32 s61, s61, 2
	s_add_u32 s22, s22, 0x100
	s_addc_u32 s23, s23, 0
	s_add_u32 s51, s51, 0x100
	s_addc_u32 s60, s60, 0
	s_cmp_gt_u32 s61, 13
	s_cbranch_scc0 .LBB0_1279
	s_and_b64 vcc, exec, s[8:9]
	s_cbranch_vccz .LBB0_1282
	s_barrier

.LBB0_1391:
	ds_read_b128 v[24:27], v186
	ds_read_b128 v[28:31], v186 offset:1024
	ds_read_b128 v[16:19], v186 offset:2048
	ds_read_b128 v[20:23], v186 offset:3072
	ds_read_b128 v[8:11], v187
	ds_read_b128 v[12:15], v187 offset:1024
	ds_read_b128 v[0:3], v187 offset:2048
	ds_read_b128 v[4:7], v187 offset:3072
	s_add_u32 s26, s24, 0xfff20080
	s_addc_u32 s27, s25, -1
	s_cmp_eq_u32 s67, 52
	s_cselect_b32 s29, s23, s27
	s_cselect_b32 s28, s22, s26
	s_cselect_b32 s27, s1, s66
	s_cselect_b32 s26, s0, s65
	s_add_i32 m0, s36, 0xc000
	ds_read_b128 v[174:177], v188
	ds_read_b128 v[178:181], v188 offset:1024
	ds_read_b128 v[192:195], v188 offset:2048
	ds_read_b128 v[196:199], v188 offset:3072
	ds_read_b128 v[202:205], v188 offset:4096
	ds_read_b128 v[206:209], v188 offset:5120
	ds_read_b128 v[210:213], v188 offset:6144
	ds_read_b128 v[214:217], v188 offset:7168
	global_load_lds_dwordx4 v170, s[24:25]
	s_add_i32 m0, s36, 0xe000
	s_nop 0
	global_load_lds_dwordx4 v172, s[24:25]
	s_waitcnt vmcnt(8)
	s_waitcnt lgkmcnt(0)
	s_barrier
	s_setprio 1
	s_waitcnt lgkmcnt(0)
	v_mfma_scale_f32_16x16x128_f8f6f4 v[156:159], v[24:31], v[174:181], v[156:159], v189, v190 op_sel_hi:[0,0,0]
	v_mfma_scale_f32_16x16x128_f8f6f4 v[152:155], v[16:23], v[174:181], v[152:155], v189, v190 op_sel_hi:[0,0,0]
	v_mfma_scale_f32_16x16x128_f8f6f4 v[140:143], v[24:31], v[192:199], v[140:143], v189, v190 op_sel_hi:[0,0,0]
	v_mfma_scale_f32_16x16x128_f8f6f4 v[136:139], v[16:23], v[192:199], v[136:139], v189, v190 op_sel_hi:[0,0,0]
	v_mfma_scale_f32_16x16x128_f8f6f4 v[124:127], v[24:31], v[202:209], v[124:127], v189, v190 op_sel_hi:[0,0,0]
	v_mfma_scale_f32_16x16x128_f8f6f4 v[120:123], v[16:23], v[202:209], v[120:123], v189, v190 op_sel_hi:[0,0,0]
	v_mfma_scale_f32_16x16x128_f8f6f4 v[108:111], v[24:31], v[210:217], v[108:111], v189, v190 op_sel_hi:[0,0,0]
	v_mfma_scale_f32_16x16x128_f8f6f4 v[104:107], v[16:23], v[210:217], v[104:107], v189, v190 op_sel_hi:[0,0,0]
	v_mfma_scale_f32_16x16x128_f8f6f4 v[148:151], v[8:15], v[174:181], v[148:151], v189, v190 op_sel_hi:[0,0,0]
	v_mfma_scale_f32_16x16x128_f8f6f4 v[144:147], v[0:7], v[174:181], v[144:147], v189, v190 op_sel_hi:[0,0,0]
	v_mfma_scale_f32_16x16x128_f8f6f4 v[132:135], v[8:15], v[192:199], v[132:135], v189, v190 op_sel_hi:[0,0,0]
	v_mfma_scale_f32_16x16x128_f8f6f4 v[128:131], v[0:7], v[192:199], v[128:131], v189, v190 op_sel_hi:[0,0,0]
	v_mfma_scale_f32_16x16x128_f8f6f4 v[116:119], v[8:15], v[202:209], v[116:119], v189, v190 op_sel_hi:[0,0,0]
	v_mfma_scale_f32_16x16x128_f8f6f4 v[112:115], v[0:7], v[202:209], v[112:115], v189, v190 op_sel_hi:[0,0,0]
	v_mfma_scale_f32_16x16x128_f8f6f4 v[100:103], v[8:15], v[210:217], v[100:103], v189, v190 op_sel_hi:[0,0,0]
	v_mfma_scale_f32_16x16x128_f8f6f4 v[96:99], v[0:7], v[210:217], v[96:99], v189, v190 op_sel_hi:[0,0,0]
	s_setprio 0
	s_barrier
	s_add_i32 s68, s44, s35
	v_lshl_add_u64 v[174:175], s[26:27], 0, v[160:161]
	s_mov_b32 m0, s68
	ds_read_b128 v[192:195], v188 offset:16384
	ds_read_b128 v[196:199], v188 offset:17408
	ds_read_b128 v[202:205], v188 offset:18432
	ds_read_b128 v[206:209], v188 offset:19456
	ds_read_b128 v[210:213], v188 offset:20480
	ds_read_b128 v[214:217], v188 offset:21504
	ds_read_b128 v[218:221], v188 offset:22528
	ds_read_b128 v[222:225], v188 offset:23552
	global_load_lds_dwordx4 v160, s[26:27]
	s_add_i32 m0, s68, 0x2000
	s_add_u32 s68, s26, 0xe0000
	v_lshl_add_u64 v[176:177], s[26:27], 0, v[164:165]
	s_addc_u32 s69, s27, 0
	s_add_i32 s70, s45, s35
	global_load_lds_dwordx4 v164, s[26:27]
	s_mov_b32 m0, s70
	v_lshl_add_u64 v[180:181], s[28:29], 0, v[166:167]
	global_load_lds_dwordx4 v160, s[68:69]
	s_add_i32 m0, s70, 0x2000
	s_nop 0
	global_load_lds_dwordx4 v164, s[68:69]
	v_lshl_add_u64 v[178:179], s[28:29], 0, v[168:169]
	s_mov_b32 m0, s36
	s_nop 0
	global_load_lds_dwordx4 v168, s[28:29]
	s_mov_b32 m0, s37
	s_nop 0
	global_load_lds_dwordx4 v166, s[28:29]
	s_waitcnt vmcnt(8)
	s_waitcnt lgkmcnt(0)
	s_barrier
	s_setprio 1
	s_waitcnt lgkmcnt(0)
	v_mfma_scale_f32_16x16x128_f8f6f4 v[92:95], v[24:31], v[192:199], v[92:95], v189, v190 op_sel_hi:[0,0,0]
	v_mfma_scale_f32_16x16x128_f8f6f4 v[88:91], v[16:23], v[192:199], v[88:91], v189, v190 op_sel_hi:[0,0,0]
	v_mfma_scale_f32_16x16x128_f8f6f4 v[76:79], v[24:31], v[202:209], v[76:79], v189, v190 op_sel_hi:[0,0,0]
	v_mfma_scale_f32_16x16x128_f8f6f4 v[72:75], v[16:23], v[202:209], v[72:75], v189, v190 op_sel_hi:[0,0,0]
	v_mfma_scale_f32_16x16x128_f8f6f4 v[60:63], v[24:31], v[210:217], v[60:63], v189, v190 op_sel_hi:[0,0,0]
	v_mfma_scale_f32_16x16x128_f8f6f4 v[56:59], v[16:23], v[210:217], v[56:59], v189, v190 op_sel_hi:[0,0,0]
	v_mfma_scale_f32_16x16x128_f8f6f4 v[44:47], v[24:31], v[218:225], v[44:47], v189, v190 op_sel_hi:[0,0,0]
	v_mfma_scale_f32_16x16x128_f8f6f4 v[40:43], v[16:23], v[218:225], v[40:43], v189, v190 op_sel_hi:[0,0,0]
	v_mfma_scale_f32_16x16x128_f8f6f4 v[84:87], v[8:15], v[192:199], v[84:87], v189, v190 op_sel_hi:[0,0,0]
	v_mfma_scale_f32_16x16x128_f8f6f4 v[80:83], v[0:7], v[192:199], v[80:83], v189, v190 op_sel_hi:[0,0,0]
	v_mfma_scale_f32_16x16x128_f8f6f4 v[68:71], v[8:15], v[202:209], v[68:71], v189, v190 op_sel_hi:[0,0,0]
	v_mfma_scale_f32_16x16x128_f8f6f4 v[64:67], v[0:7], v[202:209], v[64:67], v189, v190 op_sel_hi:[0,0,0]
	v_mfma_scale_f32_16x16x128_f8f6f4 v[52:55], v[8:15], v[210:217], v[52:55], v189, v190 op_sel_hi:[0,0,0]
	v_mfma_scale_f32_16x16x128_f8f6f4 v[48:51], v[0:7], v[210:217], v[48:51], v189, v190 op_sel_hi:[0,0,0]
	v_mfma_scale_f32_16x16x128_f8f6f4 v[36:39], v[8:15], v[218:225], v[36:39], v189, v190 op_sel_hi:[0,0,0]
	v_mfma_scale_f32_16x16x128_f8f6f4 v[32:35], v[0:7], v[218:225], v[32:35], v189, v190 op_sel_hi:[0,0,0]
	s_setprio 0
	s_barrier
	s_add_i32 s68, 0, 0x18000
	s_add_i32 s69, 0, 0x1c000
	v_add_u32_e32 v12, s68, v184
	v_add_u32_e32 v28, s69, v184
	ds_read_b128 v[0:3], v12
	ds_read_b128 v[4:7], v12 offset:1024
	ds_read_b128 v[8:11], v12 offset:2048
	ds_read_b128 v[12:15], v12 offset:3072
	ds_read_b128 v[16:19], v28
	ds_read_b128 v[20:23], v28 offset:1024
	ds_read_b128 v[24:27], v28 offset:2048
	ds_read_b128 v[28:31], v28 offset:3072
	s_add_u32 s28, s28, 0xe0000
	s_addc_u32 s29, s29, 0
	s_mov_b32 m0, s38
	ds_read_b128 v[192:195], v188 offset:32768
	ds_read_b128 v[196:199], v188 offset:33792
	ds_read_b128 v[202:205], v188 offset:34816
	ds_read_b128 v[206:209], v188 offset:35840
	ds_read_b128 v[210:213], v188 offset:36864
	ds_read_b128 v[214:217], v188 offset:37888
	ds_read_b128 v[218:221], v188 offset:38912
	ds_read_b128 v[222:225], v188 offset:39936
	global_load_lds_dwordx4 v168, s[28:29]
	s_mov_b32 m0, s39
	s_nop 0
	global_load_lds_dwordx4 v166, s[28:29]
	s_waitcnt vmcnt(8)
	s_waitcnt lgkmcnt(0)
	s_barrier
	s_setprio 1
	s_waitcnt lgkmcnt(0)
	v_mfma_scale_f32_16x16x128_f8f6f4 v[156:159], v[0:7], v[192:199], v[156:159], v189, v190 op_sel_hi:[0,0,0]
	v_mfma_scale_f32_16x16x128_f8f6f4 v[152:155], v[8:15], v[192:199], v[152:155], v189, v190 op_sel_hi:[0,0,0]
	v_mfma_scale_f32_16x16x128_f8f6f4 v[140:143], v[0:7], v[202:209], v[140:143], v189, v190 op_sel_hi:[0,0,0]
	v_mfma_scale_f32_16x16x128_f8f6f4 v[136:139], v[8:15], v[202:209], v[136:139], v189, v190 op_sel_hi:[0,0,0]
	v_mfma_scale_f32_16x16x128_f8f6f4 v[124:127], v[0:7], v[210:217], v[124:127], v189, v190 op_sel_hi:[0,0,0]
	v_mfma_scale_f32_16x16x128_f8f6f4 v[120:123], v[8:15], v[210:217], v[120:123], v189, v190 op_sel_hi:[0,0,0]
	v_mfma_scale_f32_16x16x128_f8f6f4 v[108:111], v[0:7], v[218:225], v[108:111], v189, v190 op_sel_hi:[0,0,0]
	v_mfma_scale_f32_16x16x128_f8f6f4 v[104:107], v[8:15], v[218:225], v[104:107], v189, v190 op_sel_hi:[0,0,0]
	v_mfma_scale_f32_16x16x128_f8f6f4 v[148:151], v[16:23], v[192:199], v[148:151], v189, v190 op_sel_hi:[0,0,0]
	v_mfma_scale_f32_16x16x128_f8f6f4 v[144:147], v[24:31], v[192:199], v[144:147], v189, v190 op_sel_hi:[0,0,0]
	v_mfma_scale_f32_16x16x128_f8f6f4 v[132:135], v[16:23], v[202:209], v[132:135], v189, v190 op_sel_hi:[0,0,0]
	v_mfma_scale_f32_16x16x128_f8f6f4 v[128:131], v[24:31], v[202:209], v[128:131], v189, v190 op_sel_hi:[0,0,0]
	v_mfma_scale_f32_16x16x128_f8f6f4 v[116:119], v[16:23], v[210:217], v[116:119], v189, v190 op_sel_hi:[0,0,0]
	v_mfma_scale_f32_16x16x128_f8f6f4 v[112:115], v[24:31], v[210:217], v[112:115], v189, v190 op_sel_hi:[0,0,0]
	v_mfma_scale_f32_16x16x128_f8f6f4 v[100:103], v[16:23], v[218:225], v[100:103], v189, v190 op_sel_hi:[0,0,0]
	v_mfma_scale_f32_16x16x128_f8f6f4 v[96:99], v[24:31], v[218:225], v[96:99], v189, v190 op_sel_hi:[0,0,0]
	s_setprio 0
	s_barrier
	s_add_i32 s28, s68, s35
	v_lshl_add_u64 v[174:175], v[174:175], 0, s[8:9]
	s_mov_b32 m0, s28
	ds_read_b128 v[192:195], v188 offset:49152
	ds_read_b128 v[196:199], v188 offset:50176
	ds_read_b128 v[202:205], v188 offset:51200
	ds_read_b128 v[206:209], v188 offset:52224
	ds_read_b128 v[210:213], v188 offset:53248
	ds_read_b128 v[214:217], v188 offset:54272
	ds_read_b128 v[218:221], v188 offset:55296
	ds_read_b128 v[222:225], v188 offset:56320
	global_load_lds_dwordx4 v[174:175], off
	s_add_i32 m0, s28, 0x2000
	s_add_u32 s26, s26, 0xe0080
	v_lshl_add_u64 v[174:175], v[176:177], 0, s[8:9]
	s_addc_u32 s27, s27, 0
	s_add_i32 s28, s69, s35
	global_load_lds_dwordx4 v[174:175], off
	s_mov_b32 m0, s28
	s_nop 0
	global_load_lds_dwordx4 v160, s[26:27]
	s_add_i32 m0, s28, 0x2000
	s_nop 0
	global_load_lds_dwordx4 v164, s[26:27]
	v_lshl_add_u64 v[174:175], v[178:179], 0, s[8:9]
	s_mov_b32 m0, s41
	s_nop 0
	global_load_lds_dwordx4 v[174:175], off
	v_lshl_add_u64 v[174:175], v[180:181], 0, s[8:9]
	s_mov_b32 m0, s42
	s_nop 0
	global_load_lds_dwordx4 v[174:175], off
	s_waitcnt vmcnt(8)
	s_waitcnt lgkmcnt(0)
	s_barrier
	s_setprio 1
	s_waitcnt lgkmcnt(0)
	v_mfma_scale_f32_16x16x128_f8f6f4 v[92:95], v[0:7], v[192:199], v[92:95], v189, v190 op_sel_hi:[0,0,0]
	v_mfma_scale_f32_16x16x128_f8f6f4 v[88:91], v[8:15], v[192:199], v[88:91], v189, v190 op_sel_hi:[0,0,0]
	v_mfma_scale_f32_16x16x128_f8f6f4 v[76:79], v[0:7], v[202:209], v[76:79], v189, v190 op_sel_hi:[0,0,0]
	v_mfma_scale_f32_16x16x128_f8f6f4 v[72:75], v[8:15], v[202:209], v[72:75], v189, v190 op_sel_hi:[0,0,0]
	v_mfma_scale_f32_16x16x128_f8f6f4 v[60:63], v[0:7], v[210:217], v[60:63], v189, v190 op_sel_hi:[0,0,0]
	v_mfma_scale_f32_16x16x128_f8f6f4 v[56:59], v[8:15], v[210:217], v[56:59], v189, v190 op_sel_hi:[0,0,0]
	v_mfma_scale_f32_16x16x128_f8f6f4 v[44:47], v[0:7], v[218:225], v[44:47], v189, v190 op_sel_hi:[0,0,0]
	v_mfma_scale_f32_16x16x128_f8f6f4 v[40:43], v[8:15], v[218:225], v[40:43], v189, v190 op_sel_hi:[0,0,0]
	v_mfma_scale_f32_16x16x128_f8f6f4 v[84:87], v[16:23], v[192:199], v[84:87], v189, v190 op_sel_hi:[0,0,0]
	v_mfma_scale_f32_16x16x128_f8f6f4 v[80:83], v[24:31], v[192:199], v[80:83], v189, v190 op_sel_hi:[0,0,0]
	v_mfma_scale_f32_16x16x128_f8f6f4 v[68:71], v[16:23], v[202:209], v[68:71], v189, v190 op_sel_hi:[0,0,0]
	v_mfma_scale_f32_16x16x128_f8f6f4 v[64:67], v[24:31], v[202:209], v[64:67], v189, v190 op_sel_hi:[0,0,0]
	v_mfma_scale_f32_16x16x128_f8f6f4 v[52:55], v[16:23], v[210:217], v[52:55], v189, v190 op_sel_hi:[0,0,0]
	v_mfma_scale_f32_16x16x128_f8f6f4 v[48:51], v[24:31], v[210:217], v[48:51], v189, v190 op_sel_hi:[0,0,0]
	v_mfma_scale_f32_16x16x128_f8f6f4 v[36:39], v[16:23], v[218:225], v[36:39], v189, v190 op_sel_hi:[0,0,0]
	v_mfma_scale_f32_16x16x128_f8f6f4 v[32:35], v[24:31], v[218:225], v[32:35], v189, v190 op_sel_hi:[0,0,0]
	s_setprio 0
	s_barrier
	s_add_i32 s67, s67, 2
	s_add_u32 s24, s24, 0x100
	s_addc_u32 s25, s25, 0
	s_add_u32 s65, s65, 0x100
	s_addc_u32 s66, s66, 0
	s_cmp_gt_u32 s67, 53
	s_cbranch_scc0 .LBB0_1391
	s_and_b64 vcc, exec, s[10:11]
	s_cbranch_vccz .LBB0_1394
	s_barrier
